# router phase: row sum-of-squares wait moved to its first consumer and the two bias loads hoisted to the loop head (no load-then-wait before the top-k), on top of v101
# speedup vs baseline: 1.0005x; 1.0005x over previous
.LBB0_1231:
	s_and_saveexec_b64 s[8:9], s[2:3]
	ds_write_b32 v220, v201 offset:20480
	s_or_b64 exec, exec, s[8:9]
	v_ashrrev_i32_e32 v213, 31, v212
	v_lshl_add_u64 v[0:1], v[212:213], 2, s[20:21]
	s_load_dwordx2 s[98:99], s[14:15], 0xe8
	s_waitcnt vmcnt(0) lgkmcnt(0)
	s_barrier
	global_load_dword v228, v[0:1], off
	global_load_dwordx4 v[232:235], v223, s[98:99]
	global_load_dwordx4 v[236:239], v223, s[98:99] offset:64
	v_mov_b32_e32 v226, 0
	v_mov_b32_e32 v227, 0
	v_lshlrev_b64 v[218:219], 10, v[212:213]
	v_lshl_add_u64 v[218:219], v[208:209], 0, v[218:219]
	v_lshlrev_b64 v[0:1], 11, v[212:213]
	v_lshl_add_u64 v[0:1], v[202:203], 0, v[0:1]
	global_load_dwordx4 v[196:199], v[0:1], off
	global_load_dwordx4 v[192:195], v[0:1], off offset:64
	global_load_dwordx4 v[188:191], v[0:1], off offset:128
	global_load_dwordx4 v[184:187], v[0:1], off offset:192
	global_load_dwordx4 v[180:183], v[0:1], off offset:256
	global_load_dwordx4 v[176:179], v[0:1], off offset:320
	global_load_dwordx4 v[172:175], v[0:1], off offset:384
	global_load_dwordx4 v[168:171], v[0:1], off offset:448
	global_load_dwordx4 v[164:167], v[0:1], off offset:512
	global_load_dwordx4 v[160:163], v[0:1], off offset:576
	global_load_dwordx4 v[156:159], v[0:1], off offset:640
	global_load_dwordx4 v[152:155], v[0:1], off offset:704
	global_load_dwordx4 v[148:151], v[0:1], off offset:768
	global_load_dwordx4 v[144:147], v[0:1], off offset:832
	global_load_dwordx4 v[140:143], v[0:1], off offset:896
	global_load_dwordx4 v[136:139], v[0:1], off offset:960
	global_load_dwordx4 v[132:135], v[0:1], off offset:1024
	global_load_dwordx4 v[128:131], v[0:1], off offset:1088
	global_load_dwordx4 v[124:127], v[0:1], off offset:1152
	global_load_dwordx4 v[120:123], v[0:1], off offset:1216
	global_load_dwordx4 v[116:119], v[0:1], off offset:1280
	global_load_dwordx4 v[112:115], v[0:1], off offset:1344
	global_load_dwordx4 v[108:111], v[0:1], off offset:1408
	global_load_dwordx4 v[100:103], v[0:1], off offset:1472
	global_load_dwordx4 v[28:31], v[0:1], off offset:1536
	global_load_dwordx4 v[24:27], v[0:1], off offset:1600
	global_load_dwordx4 v[20:23], v[0:1], off offset:1664
	global_load_dwordx4 v[16:19], v[0:1], off offset:1728
	global_load_dwordx4 v[12:15], v[0:1], off offset:1792
	global_load_dwordx4 v[8:11], v[0:1], off offset:1856
	global_load_dwordx4 v[4:7], v[0:1], off offset:1920
	s_nop 0
	global_load_dwordx4 v[0:3], v[0:1], off offset:1984
	s_nop 0
	global_load_dwordx4 v[32:35], v[204:205], off
	global_load_dwordx4 v[36:39], v[206:207], off
	global_load_dwordx4 v[40:43], v[204:205], off offset:64
	global_load_dwordx4 v[44:47], v[206:207], off offset:64
	global_load_dwordx4 v[48:51], v[204:205], off offset:128
	global_load_dwordx4 v[52:55], v[206:207], off offset:128
	global_load_dwordx4 v[56:59], v[204:205], off offset:192
	global_load_dwordx4 v[60:63], v[206:207], off offset:192
	global_load_dwordx4 v[64:67], v[204:205], off offset:256
	global_load_dwordx4 v[68:71], v[206:207], off offset:256
	global_load_dwordx4 v[72:75], v[204:205], off offset:320
	global_load_dwordx4 v[76:79], v[206:207], off offset:320
	global_load_dwordx4 v[80:83], v[204:205], off offset:384
	global_load_dwordx4 v[84:87], v[206:207], off offset:384
	global_load_dwordx4 v[88:91], v[204:205], off offset:448
	global_load_dwordx4 v[92:95], v[206:207], off offset:448
	s_waitcnt vmcnt(15)
	v_fmamk_f32 v228, v228, 0x3a800000, v222
	v_cmp_gt_f32_e32 vcc, s37, v228
	v_mul_f32_e32 v229, 0x4b800000, v228
	s_nop 0
	v_cndmask_b32_e32 v228, v228, v229, vcc
	v_rsq_f32_e32 v200, v228
	s_nop 0
	v_mul_f32_e32 v215, 0x45800000, v200
	v_cndmask_b32_e32 v216, v200, v215, vcc
	v_mfma_f32_16x16x32_bf16 v[32:35], v[32:35], v[196:199], 0
	v_lshlrev_b32_e32 v200, 16, v196
	v_mul_f32_e32 v200, v216, v200
	v_lshlrev_b32_e32 v213, 16, v197
	s_waitcnt vmcnt(14)
	v_mfma_f32_16x16x32_bf16 v[36:39], v[36:39], v[196:199], 0
	v_and_b32_e32 v196, 0xffff0000, v196
	v_mul_f32_e32 v196, v216, v196
	v_cvt_pk_fp8_f32 v226, v200, v196
	s_waitcnt vmcnt(13)
	v_mfma_f32_16x16x32_bf16 v[32:35], v[40:43], v[192:195], v[32:35]
	v_lshlrev_b32_e32 v196, 16, v198
	v_and_b32_e32 v198, 0xffff0000, v198
	v_mul_f32_e32 v196, v216, v196
	s_waitcnt vmcnt(12)
	v_mfma_f32_16x16x32_bf16 v[36:39], v[44:47], v[192:195], v[36:39]
	v_mul_f32_e32 v198, v216, v198
	v_cvt_pk_fp8_f32 v227, v196, v198
	v_lshlrev_b32_e32 v200, 16, v199
	s_waitcnt vmcnt(11)
	v_mfma_f32_16x16x32_bf16 v[32:35], v[48:51], v[188:191], v[32:35]
	v_and_b32_e32 v199, 0xffff0000, v199
	v_lshlrev_b32_e32 v196, 16, v192
	v_and_b32_e32 v192, 0xffff0000, v192
	s_waitcnt vmcnt(10)
	v_mfma_f32_16x16x32_bf16 v[36:39], v[52:55], v[188:191], v[36:39]
	v_mul_f32_e32 v200, v216, v200
	v_mul_f32_e32 v199, v216, v199
	v_mul_f32_e32 v198, v216, v192
	s_waitcnt vmcnt(9)
	v_mfma_f32_16x16x32_bf16 v[32:35], v[56:59], v[184:187], v[32:35]
	v_lshlrev_b32_e32 v192, 16, v193
	v_cvt_pk_fp8_f32 v227, v200, v199 op_sel:[0,0,1]
	v_mul_f32_e32 v199, v216, v192
	s_waitcnt vmcnt(8)
	v_mfma_f32_16x16x32_bf16 v[36:39], v[60:63], v[184:187], v[36:39]
	v_and_b32_e32 v192, 0xffff0000, v193
	v_mul_f32_e32 v196, v216, v196
	v_mul_f32_e32 v193, v216, v192
	s_waitcnt vmcnt(7)
	v_mfma_f32_16x16x32_bf16 v[32:35], v[64:67], v[180:183], v[32:35]
	v_mov_b32_e32 v192, 0
	v_cvt_pk_fp8_f32 v192, v196, v198
	v_and_b32_e32 v197, 0xffff0000, v197
	s_waitcnt vmcnt(6)
	v_mfma_f32_16x16x32_bf16 v[36:39], v[68:71], v[180:183], v[36:39]
	v_mul_f32_e32 v213, v216, v213
	v_cvt_pk_fp8_f32 v192, v199, v193 op_sel:[0,0,1]
	v_lshlrev_b32_e32 v193, 16, v194
	s_waitcnt vmcnt(5)
	v_mfma_f32_16x16x32_bf16 v[32:35], v[72:75], v[176:179], v[32:35]
	v_mul_f32_e32 v196, v216, v193
	v_and_b32_e32 v193, 0xffff0000, v194
	v_mul_f32_e32 v194, v216, v193
	s_waitcnt vmcnt(4)
	v_mfma_f32_16x16x32_bf16 v[36:39], v[76:79], v[176:179], v[36:39]
	v_lshlrev_b32_e32 v193, 16, v195
	v_mul_f32_e32 v198, v216, v193
	v_and_b32_e32 v193, 0xffff0000, v195
	s_waitcnt vmcnt(3)
	v_mfma_f32_16x16x32_bf16 v[32:35], v[80:83], v[172:175], v[32:35]
	v_mul_f32_e32 v195, v216, v193
	v_mov_b32_e32 v193, 0
	v_cvt_pk_fp8_f32 v193, v196, v194
	s_waitcnt vmcnt(2)
	v_mfma_f32_16x16x32_bf16 v[36:39], v[84:87], v[172:175], v[36:39]
	v_mul_f32_e32 v215, v216, v197
	v_cvt_pk_fp8_f32 v226, v213, v215 op_sel:[0,0,1]
	v_cvt_pk_fp8_f32 v193, v198, v195 op_sel:[0,0,1]
	s_waitcnt vmcnt(1)
	v_mfma_f32_16x16x32_bf16 v[32:35], v[88:91], v[168:171], v[32:35]
	v_mov_b32_e32 v197, 0
	v_mov_b32_e32 v196, 0
	v_mov_b32_e32 v200, 0
	s_waitcnt vmcnt(0)
	v_mfma_f32_16x16x32_bf16 v[36:39], v[92:95], v[168:171], v[36:39]
	global_load_dwordx4 v[40:43], v[204:205], off offset:512
	global_load_dwordx4 v[44:47], v[206:207], off offset:512
	global_load_dwordx4 v[48:51], v[204:205], off offset:576
	global_load_dwordx4 v[52:55], v[206:207], off offset:576
	global_load_dwordx4 v[56:59], v[204:205], off offset:640
	global_load_dwordx4 v[60:63], v[206:207], off offset:640
	global_load_dwordx4 v[64:67], v[204:205], off offset:704
	global_load_dwordx4 v[68:71], v[206:207], off offset:704
	global_load_dwordx4 v[72:75], v[204:205], off offset:768
	global_load_dwordx4 v[76:79], v[206:207], off offset:768
	global_load_dwordx4 v[80:83], v[204:205], off offset:832
	global_load_dwordx4 v[84:87], v[206:207], off offset:832
	global_load_dwordx4 v[88:91], v[204:205], off offset:896
	global_load_dwordx4 v[92:95], v[206:207], off offset:896
	global_load_dwordx4 v[96:99], v[204:205], off offset:960
	global_load_dwordx4 v[104:107], v[206:207], off offset:960
	s_waitcnt vmcnt(15)
	v_mfma_f32_16x16x32_bf16 v[32:35], v[40:43], v[164:167], v[32:35]
	s_waitcnt vmcnt(14)
	v_mfma_f32_16x16x32_bf16 v[36:39], v[44:47], v[164:167], v[36:39]
	s_waitcnt vmcnt(13)
	v_mfma_f32_16x16x32_bf16 v[32:35], v[48:51], v[160:163], v[32:35]
	s_waitcnt vmcnt(12)
	v_mfma_f32_16x16x32_bf16 v[36:39], v[52:55], v[160:163], v[36:39]
	s_waitcnt vmcnt(11)
	v_mfma_f32_16x16x32_bf16 v[32:35], v[56:59], v[156:159], v[32:35]
	s_waitcnt vmcnt(10)
	v_mfma_f32_16x16x32_bf16 v[36:39], v[60:63], v[156:159], v[36:39]
	s_waitcnt vmcnt(9)
	v_mfma_f32_16x16x32_bf16 v[32:35], v[64:67], v[152:155], v[32:35]
	s_waitcnt vmcnt(8)
	v_mfma_f32_16x16x32_bf16 v[36:39], v[68:71], v[152:155], v[36:39]
	s_waitcnt vmcnt(7)
	v_mfma_f32_16x16x32_bf16 v[32:35], v[72:75], v[148:151], v[32:35]
	s_waitcnt vmcnt(6)
	v_mfma_f32_16x16x32_bf16 v[36:39], v[76:79], v[148:151], v[36:39]
	s_waitcnt vmcnt(5)
	v_mfma_f32_16x16x32_bf16 v[32:35], v[80:83], v[144:147], v[32:35]
	s_waitcnt vmcnt(4)
	v_mfma_f32_16x16x32_bf16 v[36:39], v[84:87], v[144:147], v[36:39]
	s_waitcnt vmcnt(3)
	v_mfma_f32_16x16x32_bf16 v[32:35], v[88:91], v[140:143], v[32:35]
	s_waitcnt vmcnt(2)
	v_mfma_f32_16x16x32_bf16 v[36:39], v[92:95], v[140:143], v[36:39]
	s_waitcnt vmcnt(1)
	v_mfma_f32_16x16x32_bf16 v[32:35], v[96:99], v[136:139], v[32:35]
	s_waitcnt vmcnt(0)
	v_mfma_f32_16x16x32_bf16 v[36:39], v[104:107], v[136:139], v[36:39]
	global_load_dwordx4 v[40:43], v[204:205], off offset:1024
	global_load_dwordx4 v[44:47], v[206:207], off offset:1024
	global_load_dwordx4 v[48:51], v[204:205], off offset:1088
	global_load_dwordx4 v[52:55], v[206:207], off offset:1088
	global_load_dwordx4 v[56:59], v[204:205], off offset:1152
	global_load_dwordx4 v[60:63], v[206:207], off offset:1152
	global_load_dwordx4 v[64:67], v[204:205], off offset:1216
	global_load_dwordx4 v[68:71], v[206:207], off offset:1216
	global_load_dwordx4 v[72:75], v[204:205], off offset:1280
	global_load_dwordx4 v[76:79], v[206:207], off offset:1280
	global_load_dwordx4 v[80:83], v[204:205], off offset:1344
	global_load_dwordx4 v[84:87], v[206:207], off offset:1344
	global_load_dwordx4 v[88:91], v[204:205], off offset:1408
	global_load_dwordx4 v[92:95], v[206:207], off offset:1408
	global_load_dwordx4 v[96:99], v[204:205], off offset:1472
	global_load_dwordx4 v[104:107], v[206:207], off offset:1472
	s_waitcnt vmcnt(15)
	v_mfma_f32_16x16x32_bf16 v[32:35], v[40:43], v[132:135], v[32:35]
	s_waitcnt vmcnt(14)
	v_mfma_f32_16x16x32_bf16 v[36:39], v[44:47], v[132:135], v[36:39]
	s_waitcnt vmcnt(13)
	v_mfma_f32_16x16x32_bf16 v[32:35], v[48:51], v[128:131], v[32:35]
	s_waitcnt vmcnt(12)
	v_mfma_f32_16x16x32_bf16 v[36:39], v[52:55], v[128:131], v[36:39]
	s_waitcnt vmcnt(11)
	v_mfma_f32_16x16x32_bf16 v[32:35], v[56:59], v[124:127], v[32:35]
	s_waitcnt vmcnt(10)
	v_mfma_f32_16x16x32_bf16 v[36:39], v[60:63], v[124:127], v[36:39]
	s_waitcnt vmcnt(9)
	v_mfma_f32_16x16x32_bf16 v[32:35], v[64:67], v[120:123], v[32:35]
	s_waitcnt vmcnt(8)
	v_mfma_f32_16x16x32_bf16 v[36:39], v[68:71], v[120:123], v[36:39]
	s_waitcnt vmcnt(7)
	v_mfma_f32_16x16x32_bf16 v[32:35], v[72:75], v[116:119], v[32:35]
	s_waitcnt vmcnt(6)
	v_mfma_f32_16x16x32_bf16 v[36:39], v[76:79], v[116:119], v[36:39]
	s_waitcnt vmcnt(5)
	v_mfma_f32_16x16x32_bf16 v[32:35], v[80:83], v[112:115], v[32:35]
	s_waitcnt vmcnt(4)
	v_mfma_f32_16x16x32_bf16 v[36:39], v[84:87], v[112:115], v[36:39]
	s_waitcnt vmcnt(3)
	v_mfma_f32_16x16x32_bf16 v[32:35], v[88:91], v[108:111], v[32:35]
	s_waitcnt vmcnt(2)
	v_mfma_f32_16x16x32_bf16 v[36:39], v[92:95], v[108:111], v[36:39]
	s_waitcnt vmcnt(1)
	v_mfma_f32_16x16x32_bf16 v[72:75], v[96:99], v[100:103], v[32:35]
	s_waitcnt vmcnt(0)
	v_mfma_f32_16x16x32_bf16 v[64:67], v[104:107], v[100:103], v[36:39]
	global_load_dwordx4 v[104:107], v[204:205], off offset:1536
	global_load_dwordx4 v[96:99], v[206:207], off offset:1536
	global_load_dwordx4 v[92:95], v[204:205], off offset:1600
	global_load_dwordx4 v[88:91], v[206:207], off offset:1600
	global_load_dwordx4 v[84:87], v[204:205], off offset:1664
	global_load_dwordx4 v[80:83], v[206:207], off offset:1664
	global_load_dwordx4 v[76:79], v[204:205], off offset:1728
	global_load_dwordx4 v[68:71], v[206:207], off offset:1728
	global_load_dwordx4 v[60:63], v[204:205], off offset:1792
	global_load_dwordx4 v[56:59], v[206:207], off offset:1792
	global_load_dwordx4 v[52:55], v[204:205], off offset:1856
	global_load_dwordx4 v[48:51], v[206:207], off offset:1856
	global_load_dwordx4 v[44:47], v[204:205], off offset:1920
	global_load_dwordx4 v[32:35], v[206:207], off offset:1920
	global_load_dwordx4 v[36:39], v[204:205], off offset:1984
	global_load_dwordx4 v[40:43], v[206:207], off offset:1984
	global_store_dwordx2 v[218:219], v[192:193], off offset:32
	v_lshlrev_b32_e32 v192, 16, v188
	v_and_b32_e32 v188, 0xffff0000, v188
	v_mul_f32_e32 v193, v216, v188
	v_lshlrev_b32_e32 v188, 16, v189
	v_mul_f32_e32 v194, v216, v188
	v_and_b32_e32 v188, 0xffff0000, v189
	v_mul_f32_e32 v192, v216, v192
	v_mul_f32_e32 v189, v216, v188
	v_mov_b32_e32 v188, 0
	v_cvt_pk_fp8_f32 v188, v192, v193
	s_waitcnt vmcnt(16)
	v_mfma_f32_16x16x32_bf16 v[72:75], v[104:107], v[28:31], v[72:75]
	v_cvt_pk_fp8_f32 v188, v194, v189 op_sel:[0,0,1]
	v_lshlrev_b32_e32 v189, 16, v190
	v_mul_f32_e32 v192, v216, v189
	v_and_b32_e32 v189, 0xffff0000, v190
	v_mul_f32_e32 v190, v216, v189
	v_lshlrev_b32_e32 v189, 16, v191
	v_mul_f32_e32 v193, v216, v189
	v_and_b32_e32 v189, 0xffff0000, v191
	v_mul_f32_e32 v191, v216, v189
	v_mov_b32_e32 v189, 0
	v_cvt_pk_fp8_f32 v189, v192, v190
	global_store_dwordx2 v[218:219], v[226:227], off
	v_cvt_pk_fp8_f32 v189, v193, v191 op_sel:[0,0,1]
	global_store_dwordx2 v[218:219], v[188:189], off offset:64
	v_lshlrev_b32_e32 v188, 16, v184
	v_and_b32_e32 v184, 0xffff0000, v184
	v_mul_f32_e32 v189, v216, v184
	v_lshlrev_b32_e32 v184, 16, v185
	v_mul_f32_e32 v190, v216, v184
	v_and_b32_e32 v184, 0xffff0000, v185
	v_mul_f32_e32 v188, v216, v188
	v_mul_f32_e32 v185, v216, v184
	v_mov_b32_e32 v184, 0
	v_cvt_pk_fp8_f32 v184, v188, v189
	v_cvt_pk_fp8_f32 v184, v190, v185 op_sel:[0,0,1]
	v_lshlrev_b32_e32 v185, 16, v186
	v_mul_f32_e32 v188, v216, v185
	v_and_b32_e32 v185, 0xffff0000, v186
	v_mul_f32_e32 v186, v216, v185
	v_lshlrev_b32_e32 v185, 16, v187
	v_mul_f32_e32 v189, v216, v185
	v_and_b32_e32 v185, 0xffff0000, v187
	v_mul_f32_e32 v187, v216, v185
	v_mov_b32_e32 v185, 0
	v_cvt_pk_fp8_f32 v185, v188, v186
	v_cvt_pk_fp8_f32 v185, v189, v187 op_sel:[0,0,1]
	global_store_dwordx2 v[218:219], v[184:185], off offset:96
	v_lshlrev_b32_e32 v184, 16, v180
	v_and_b32_e32 v180, 0xffff0000, v180
	v_mul_f32_e32 v185, v216, v180
	v_lshlrev_b32_e32 v180, 16, v181
	v_mul_f32_e32 v186, v216, v180
	v_and_b32_e32 v180, 0xffff0000, v181
	v_mul_f32_e32 v184, v216, v184
	v_mul_f32_e32 v181, v216, v180
	v_mov_b32_e32 v180, 0
	v_cvt_pk_fp8_f32 v180, v184, v185
	v_cvt_pk_fp8_f32 v180, v186, v181 op_sel:[0,0,1]
	v_lshlrev_b32_e32 v181, 16, v182
	v_mul_f32_e32 v184, v216, v181
	v_and_b32_e32 v181, 0xffff0000, v182
	v_mul_f32_e32 v182, v216, v181
	v_lshlrev_b32_e32 v181, 16, v183
	v_mul_f32_e32 v185, v216, v181
	v_and_b32_e32 v181, 0xffff0000, v183
	v_mul_f32_e32 v183, v216, v181
	v_mov_b32_e32 v181, 0
	v_cvt_pk_fp8_f32 v181, v184, v182
	v_cvt_pk_fp8_f32 v181, v185, v183 op_sel:[0,0,1]
	global_store_dwordx2 v[218:219], v[180:181], off offset:128
	v_lshlrev_b32_e32 v180, 16, v176
	v_and_b32_e32 v176, 0xffff0000, v176
	v_mul_f32_e32 v181, v216, v176
	v_lshlrev_b32_e32 v176, 16, v177
	v_mul_f32_e32 v182, v216, v176
	v_and_b32_e32 v176, 0xffff0000, v177
	v_mul_f32_e32 v180, v216, v180
	v_mul_f32_e32 v177, v216, v176
	v_mov_b32_e32 v176, 0
	v_cvt_pk_fp8_f32 v176, v180, v181
	v_cvt_pk_fp8_f32 v176, v182, v177 op_sel:[0,0,1]
	v_lshlrev_b32_e32 v177, 16, v178
	v_mul_f32_e32 v180, v216, v177
	v_and_b32_e32 v177, 0xffff0000, v178
	v_mul_f32_e32 v178, v216, v177
	v_lshlrev_b32_e32 v177, 16, v179
	v_mul_f32_e32 v181, v216, v177
	v_and_b32_e32 v177, 0xffff0000, v179
	v_mul_f32_e32 v179, v216, v177
	v_mov_b32_e32 v177, 0
	v_cvt_pk_fp8_f32 v177, v180, v178
	v_cvt_pk_fp8_f32 v177, v181, v179 op_sel:[0,0,1]
	global_store_dwordx2 v[218:219], v[176:177], off offset:160
	v_lshlrev_b32_e32 v176, 16, v172
	v_and_b32_e32 v172, 0xffff0000, v172
	v_mul_f32_e32 v177, v216, v172
	v_lshlrev_b32_e32 v172, 16, v173
	v_mul_f32_e32 v178, v216, v172
	v_and_b32_e32 v172, 0xffff0000, v173
	v_mul_f32_e32 v176, v216, v176
	v_mul_f32_e32 v173, v216, v172
	v_mov_b32_e32 v172, 0
	v_cvt_pk_fp8_f32 v172, v176, v177
	v_cvt_pk_fp8_f32 v172, v178, v173 op_sel:[0,0,1]
	v_lshlrev_b32_e32 v173, 16, v174
	v_mul_f32_e32 v176, v216, v173
	v_and_b32_e32 v173, 0xffff0000, v174
	v_mul_f32_e32 v174, v216, v173
	v_lshlrev_b32_e32 v173, 16, v175
	v_mul_f32_e32 v177, v216, v173
	v_and_b32_e32 v173, 0xffff0000, v175
	v_mul_f32_e32 v175, v216, v173
	v_mov_b32_e32 v173, 0
	v_cvt_pk_fp8_f32 v173, v176, v174
	v_cvt_pk_fp8_f32 v173, v177, v175 op_sel:[0,0,1]
	global_store_dwordx2 v[218:219], v[172:173], off offset:192
	v_lshlrev_b32_e32 v172, 16, v168
	v_and_b32_e32 v168, 0xffff0000, v168
	v_mul_f32_e32 v173, v216, v168
	v_lshlrev_b32_e32 v168, 16, v169
	v_mul_f32_e32 v174, v216, v168
	v_and_b32_e32 v168, 0xffff0000, v169
	v_mul_f32_e32 v172, v216, v172
	v_mul_f32_e32 v169, v216, v168
	v_mov_b32_e32 v168, 0
	v_cvt_pk_fp8_f32 v168, v172, v173
	v_cvt_pk_fp8_f32 v168, v174, v169 op_sel:[0,0,1]
	v_lshlrev_b32_e32 v169, 16, v170
	v_mul_f32_e32 v172, v216, v169
	v_and_b32_e32 v169, 0xffff0000, v170
	v_mul_f32_e32 v170, v216, v169
	v_lshlrev_b32_e32 v169, 16, v171
	v_mul_f32_e32 v173, v216, v169
	v_and_b32_e32 v169, 0xffff0000, v171
	v_mul_f32_e32 v171, v216, v169
	v_mov_b32_e32 v169, 0
	v_cvt_pk_fp8_f32 v169, v172, v170
	v_cvt_pk_fp8_f32 v169, v173, v171 op_sel:[0,0,1]
	global_store_dwordx2 v[218:219], v[168:169], off offset:224
	v_lshlrev_b32_e32 v168, 16, v164
	v_and_b32_e32 v164, 0xffff0000, v164
	v_mul_f32_e32 v169, v216, v164
	v_lshlrev_b32_e32 v164, 16, v165
	v_mul_f32_e32 v170, v216, v164
	v_and_b32_e32 v164, 0xffff0000, v165
	v_mul_f32_e32 v168, v216, v168
	v_mul_f32_e32 v165, v216, v164
	v_mov_b32_e32 v164, 0
	v_cvt_pk_fp8_f32 v164, v168, v169
	v_cvt_pk_fp8_f32 v164, v170, v165 op_sel:[0,0,1]
	v_lshlrev_b32_e32 v165, 16, v166
	v_mul_f32_e32 v168, v216, v165
	v_and_b32_e32 v165, 0xffff0000, v166
	v_mul_f32_e32 v166, v216, v165
	v_lshlrev_b32_e32 v165, 16, v167
	v_mul_f32_e32 v169, v216, v165
	v_and_b32_e32 v165, 0xffff0000, v167
	v_mul_f32_e32 v167, v216, v165
	v_mov_b32_e32 v165, 0
	v_cvt_pk_fp8_f32 v165, v168, v166
	v_cvt_pk_fp8_f32 v165, v169, v167 op_sel:[0,0,1]
	global_store_dwordx2 v[218:219], v[164:165], off offset:256
	v_lshlrev_b32_e32 v164, 16, v160
	v_and_b32_e32 v160, 0xffff0000, v160
	v_mul_f32_e32 v165, v216, v160
	v_lshlrev_b32_e32 v160, 16, v161
	v_mul_f32_e32 v166, v216, v160
	v_and_b32_e32 v160, 0xffff0000, v161
	v_mul_f32_e32 v164, v216, v164
	v_mul_f32_e32 v161, v216, v160
	v_mov_b32_e32 v160, 0
	v_cvt_pk_fp8_f32 v160, v164, v165
	v_cvt_pk_fp8_f32 v160, v166, v161 op_sel:[0,0,1]
	v_lshlrev_b32_e32 v161, 16, v162
	v_mul_f32_e32 v164, v216, v161
	v_and_b32_e32 v161, 0xffff0000, v162
	v_mul_f32_e32 v162, v216, v161
	v_lshlrev_b32_e32 v161, 16, v163
	v_mul_f32_e32 v165, v216, v161
	v_and_b32_e32 v161, 0xffff0000, v163
	v_mul_f32_e32 v163, v216, v161
	v_mov_b32_e32 v161, 0
	v_cvt_pk_fp8_f32 v161, v164, v162
	v_cvt_pk_fp8_f32 v161, v165, v163 op_sel:[0,0,1]
	global_store_dwordx2 v[218:219], v[160:161], off offset:288
	v_lshlrev_b32_e32 v160, 16, v156
	v_and_b32_e32 v156, 0xffff0000, v156
	v_mul_f32_e32 v161, v216, v156
	v_lshlrev_b32_e32 v156, 16, v157
	v_mul_f32_e32 v162, v216, v156
	v_and_b32_e32 v156, 0xffff0000, v157
	v_mul_f32_e32 v160, v216, v160
	v_mul_f32_e32 v157, v216, v156
	v_mov_b32_e32 v156, 0
	v_cvt_pk_fp8_f32 v156, v160, v161
	v_cvt_pk_fp8_f32 v156, v162, v157 op_sel:[0,0,1]
	v_lshlrev_b32_e32 v157, 16, v158
	v_mul_f32_e32 v160, v216, v157
	v_and_b32_e32 v157, 0xffff0000, v158
	v_mul_f32_e32 v158, v216, v157
	v_lshlrev_b32_e32 v157, 16, v159
	v_mul_f32_e32 v161, v216, v157
	v_and_b32_e32 v157, 0xffff0000, v159
	v_mul_f32_e32 v159, v216, v157
	v_mov_b32_e32 v157, 0
	v_cvt_pk_fp8_f32 v157, v160, v158
	v_cvt_pk_fp8_f32 v157, v161, v159 op_sel:[0,0,1]
	global_store_dwordx2 v[218:219], v[156:157], off offset:320
	v_lshlrev_b32_e32 v156, 16, v152
	v_and_b32_e32 v152, 0xffff0000, v152
	v_mul_f32_e32 v157, v216, v152
	v_lshlrev_b32_e32 v152, 16, v153
	v_mul_f32_e32 v158, v216, v152
	v_and_b32_e32 v152, 0xffff0000, v153
	v_mul_f32_e32 v156, v216, v156
	v_mul_f32_e32 v153, v216, v152
	v_mov_b32_e32 v152, 0
	v_cvt_pk_fp8_f32 v152, v156, v157
	v_cvt_pk_fp8_f32 v152, v158, v153 op_sel:[0,0,1]
	v_lshlrev_b32_e32 v153, 16, v154
	v_mul_f32_e32 v156, v216, v153
	v_and_b32_e32 v153, 0xffff0000, v154
	v_mul_f32_e32 v154, v216, v153
	v_lshlrev_b32_e32 v153, 16, v155
	v_mul_f32_e32 v157, v216, v153
	v_and_b32_e32 v153, 0xffff0000, v155
	v_mul_f32_e32 v155, v216, v153
	v_mov_b32_e32 v153, 0
	v_cvt_pk_fp8_f32 v153, v156, v154
	v_cvt_pk_fp8_f32 v153, v157, v155 op_sel:[0,0,1]
	global_store_dwordx2 v[218:219], v[152:153], off offset:352
	v_lshlrev_b32_e32 v152, 16, v148
	v_and_b32_e32 v148, 0xffff0000, v148
	v_mul_f32_e32 v153, v216, v148
	v_lshlrev_b32_e32 v148, 16, v149
	v_mul_f32_e32 v154, v216, v148
	v_and_b32_e32 v148, 0xffff0000, v149
	v_mul_f32_e32 v152, v216, v152
	v_mul_f32_e32 v149, v216, v148
	v_mov_b32_e32 v148, 0
	v_cvt_pk_fp8_f32 v148, v152, v153
	v_cvt_pk_fp8_f32 v148, v154, v149 op_sel:[0,0,1]
	v_lshlrev_b32_e32 v149, 16, v150
	v_mul_f32_e32 v152, v216, v149
	v_and_b32_e32 v149, 0xffff0000, v150
	v_mul_f32_e32 v150, v216, v149
	v_lshlrev_b32_e32 v149, 16, v151
	v_mul_f32_e32 v153, v216, v149
	v_and_b32_e32 v149, 0xffff0000, v151
	v_mul_f32_e32 v151, v216, v149
	v_mov_b32_e32 v149, 0
	v_cvt_pk_fp8_f32 v149, v152, v150
	v_cvt_pk_fp8_f32 v149, v153, v151 op_sel:[0,0,1]
	global_store_dwordx2 v[218:219], v[148:149], off offset:384
	v_lshlrev_b32_e32 v148, 16, v144
	v_and_b32_e32 v144, 0xffff0000, v144
	v_mul_f32_e32 v149, v216, v144
	v_lshlrev_b32_e32 v144, 16, v145
	v_mul_f32_e32 v150, v216, v144
	v_and_b32_e32 v144, 0xffff0000, v145
	v_mul_f32_e32 v148, v216, v148
	v_mul_f32_e32 v145, v216, v144
	v_mov_b32_e32 v144, 0
	v_cvt_pk_fp8_f32 v144, v148, v149
	v_cvt_pk_fp8_f32 v144, v150, v145 op_sel:[0,0,1]
	v_lshlrev_b32_e32 v145, 16, v146
	v_mul_f32_e32 v148, v216, v145
	v_and_b32_e32 v145, 0xffff0000, v146
	v_mul_f32_e32 v146, v216, v145
	v_lshlrev_b32_e32 v145, 16, v147
	v_mul_f32_e32 v149, v216, v145
	v_and_b32_e32 v145, 0xffff0000, v147
	v_mul_f32_e32 v147, v216, v145
	v_mov_b32_e32 v145, 0
	v_cvt_pk_fp8_f32 v145, v148, v146
	v_cvt_pk_fp8_f32 v145, v149, v147 op_sel:[0,0,1]
	global_store_dwordx2 v[218:219], v[144:145], off offset:416
	v_lshlrev_b32_e32 v144, 16, v140
	v_and_b32_e32 v140, 0xffff0000, v140
	v_mul_f32_e32 v145, v216, v140
	v_lshlrev_b32_e32 v140, 16, v141
	v_mul_f32_e32 v146, v216, v140
	v_and_b32_e32 v140, 0xffff0000, v141
	v_mul_f32_e32 v144, v216, v144
	v_mul_f32_e32 v141, v216, v140
	v_mov_b32_e32 v140, 0
	v_cvt_pk_fp8_f32 v140, v144, v145
	v_cvt_pk_fp8_f32 v140, v146, v141 op_sel:[0,0,1]
	v_lshlrev_b32_e32 v141, 16, v142
	v_mul_f32_e32 v144, v216, v141
	v_and_b32_e32 v141, 0xffff0000, v142
	v_mul_f32_e32 v142, v216, v141
	v_lshlrev_b32_e32 v141, 16, v143
	v_mul_f32_e32 v145, v216, v141
	v_and_b32_e32 v141, 0xffff0000, v143
	v_mul_f32_e32 v143, v216, v141
	v_mov_b32_e32 v141, 0
	v_cvt_pk_fp8_f32 v141, v144, v142
	v_cvt_pk_fp8_f32 v141, v145, v143 op_sel:[0,0,1]
	global_store_dwordx2 v[218:219], v[140:141], off offset:448
	v_lshlrev_b32_e32 v140, 16, v136
	v_and_b32_e32 v136, 0xffff0000, v136
	v_mul_f32_e32 v141, v216, v136
	v_lshlrev_b32_e32 v136, 16, v137
	v_mul_f32_e32 v142, v216, v136
	v_and_b32_e32 v136, 0xffff0000, v137
	v_mul_f32_e32 v140, v216, v140
	v_mul_f32_e32 v137, v216, v136
	v_mov_b32_e32 v136, 0
	v_cvt_pk_fp8_f32 v136, v140, v141
	v_cvt_pk_fp8_f32 v136, v142, v137 op_sel:[0,0,1]
	v_lshlrev_b32_e32 v137, 16, v138
	v_mul_f32_e32 v140, v216, v137
	v_and_b32_e32 v137, 0xffff0000, v138
	v_mul_f32_e32 v138, v216, v137
	v_lshlrev_b32_e32 v137, 16, v139
	v_mul_f32_e32 v141, v216, v137
	v_and_b32_e32 v137, 0xffff0000, v139
	v_mul_f32_e32 v139, v216, v137
	v_mov_b32_e32 v137, 0
	v_cvt_pk_fp8_f32 v137, v140, v138
	v_cvt_pk_fp8_f32 v137, v141, v139 op_sel:[0,0,1]
	global_store_dwordx2 v[218:219], v[136:137], off offset:480
	v_lshlrev_b32_e32 v136, 16, v132
	v_and_b32_e32 v132, 0xffff0000, v132
	v_mul_f32_e32 v137, v216, v132
	v_lshlrev_b32_e32 v132, 16, v133
	v_mul_f32_e32 v138, v216, v132
	v_and_b32_e32 v132, 0xffff0000, v133
	v_mul_f32_e32 v136, v216, v136
	v_mul_f32_e32 v133, v216, v132
	v_mov_b32_e32 v132, 0
	v_cvt_pk_fp8_f32 v132, v136, v137
	v_cvt_pk_fp8_f32 v132, v138, v133 op_sel:[0,0,1]
	v_lshlrev_b32_e32 v133, 16, v134
	v_mul_f32_e32 v136, v216, v133
	v_and_b32_e32 v133, 0xffff0000, v134
	v_mul_f32_e32 v134, v216, v133
	v_lshlrev_b32_e32 v133, 16, v135
	v_mul_f32_e32 v137, v216, v133
	v_and_b32_e32 v133, 0xffff0000, v135
	v_mul_f32_e32 v135, v216, v133
	v_mov_b32_e32 v133, 0
	v_cvt_pk_fp8_f32 v133, v136, v134
	v_cvt_pk_fp8_f32 v133, v137, v135 op_sel:[0,0,1]
	global_store_dwordx2 v[218:219], v[132:133], off offset:512
	v_lshlrev_b32_e32 v132, 16, v128
	v_and_b32_e32 v128, 0xffff0000, v128
	v_mul_f32_e32 v133, v216, v128
	v_lshlrev_b32_e32 v128, 16, v129
	v_mul_f32_e32 v134, v216, v128
	v_and_b32_e32 v128, 0xffff0000, v129
	v_mul_f32_e32 v132, v216, v132
	v_mul_f32_e32 v129, v216, v128
	v_mov_b32_e32 v128, 0
	v_cvt_pk_fp8_f32 v128, v132, v133
	v_cvt_pk_fp8_f32 v128, v134, v129 op_sel:[0,0,1]
	v_lshlrev_b32_e32 v129, 16, v130
	v_mul_f32_e32 v132, v216, v129
	v_and_b32_e32 v129, 0xffff0000, v130
	v_mul_f32_e32 v130, v216, v129
	v_lshlrev_b32_e32 v129, 16, v131
	v_mul_f32_e32 v133, v216, v129
	v_and_b32_e32 v129, 0xffff0000, v131
	v_mul_f32_e32 v131, v216, v129
	v_mov_b32_e32 v129, 0
	v_cvt_pk_fp8_f32 v129, v132, v130
	v_cvt_pk_fp8_f32 v129, v133, v131 op_sel:[0,0,1]
	global_store_dwordx2 v[218:219], v[128:129], off offset:544
	v_lshlrev_b32_e32 v128, 16, v124
	v_and_b32_e32 v124, 0xffff0000, v124
	v_mul_f32_e32 v129, v216, v124
	v_lshlrev_b32_e32 v124, 16, v125
	v_mul_f32_e32 v130, v216, v124
	v_and_b32_e32 v124, 0xffff0000, v125
	v_mul_f32_e32 v128, v216, v128
	v_mul_f32_e32 v125, v216, v124
	v_mov_b32_e32 v124, 0
	v_cvt_pk_fp8_f32 v124, v128, v129
	v_cvt_pk_fp8_f32 v124, v130, v125 op_sel:[0,0,1]
	v_lshlrev_b32_e32 v125, 16, v126
	v_mul_f32_e32 v128, v216, v125
	v_and_b32_e32 v125, 0xffff0000, v126
	v_mul_f32_e32 v126, v216, v125
	v_lshlrev_b32_e32 v125, 16, v127
	v_mul_f32_e32 v129, v216, v125
	v_and_b32_e32 v125, 0xffff0000, v127
	v_mul_f32_e32 v127, v216, v125
	v_mov_b32_e32 v125, 0
	v_cvt_pk_fp8_f32 v125, v128, v126
	v_cvt_pk_fp8_f32 v125, v129, v127 op_sel:[0,0,1]
	global_store_dwordx2 v[218:219], v[124:125], off offset:576
	v_lshlrev_b32_e32 v124, 16, v120
	v_and_b32_e32 v120, 0xffff0000, v120
	v_mul_f32_e32 v125, v216, v120
	v_lshlrev_b32_e32 v120, 16, v121
	v_mul_f32_e32 v126, v216, v120
	v_and_b32_e32 v120, 0xffff0000, v121
	v_mul_f32_e32 v124, v216, v124
	v_mul_f32_e32 v121, v216, v120
	v_mov_b32_e32 v120, 0
	v_cvt_pk_fp8_f32 v120, v124, v125
	v_cvt_pk_fp8_f32 v120, v126, v121 op_sel:[0,0,1]
	v_lshlrev_b32_e32 v121, 16, v122
	v_mul_f32_e32 v124, v216, v121
	v_and_b32_e32 v121, 0xffff0000, v122
	v_mul_f32_e32 v122, v216, v121
	v_lshlrev_b32_e32 v121, 16, v123
	v_mul_f32_e32 v125, v216, v121
	v_and_b32_e32 v121, 0xffff0000, v123
	v_mul_f32_e32 v123, v216, v121
	v_mov_b32_e32 v121, 0
	v_cvt_pk_fp8_f32 v121, v124, v122
	v_cvt_pk_fp8_f32 v121, v125, v123 op_sel:[0,0,1]
	global_store_dwordx2 v[218:219], v[120:121], off offset:608
	v_lshlrev_b32_e32 v120, 16, v116
	v_and_b32_e32 v116, 0xffff0000, v116
	v_mul_f32_e32 v121, v216, v116
	v_lshlrev_b32_e32 v116, 16, v117
	v_mul_f32_e32 v122, v216, v116
	v_and_b32_e32 v116, 0xffff0000, v117
	v_mul_f32_e32 v120, v216, v120
	v_mul_f32_e32 v117, v216, v116
	v_mov_b32_e32 v116, 0
	v_cvt_pk_fp8_f32 v116, v120, v121
	v_cvt_pk_fp8_f32 v116, v122, v117 op_sel:[0,0,1]
	v_lshlrev_b32_e32 v117, 16, v118
	v_mul_f32_e32 v120, v216, v117
	v_and_b32_e32 v117, 0xffff0000, v118
	v_mul_f32_e32 v118, v216, v117
	v_lshlrev_b32_e32 v117, 16, v119
	v_mul_f32_e32 v121, v216, v117
	v_and_b32_e32 v117, 0xffff0000, v119
	v_mul_f32_e32 v119, v216, v117
	v_mov_b32_e32 v117, 0
	v_cvt_pk_fp8_f32 v117, v120, v118
	v_cvt_pk_fp8_f32 v117, v121, v119 op_sel:[0,0,1]
	global_store_dwordx2 v[218:219], v[116:117], off offset:640
	v_lshlrev_b32_e32 v116, 16, v112
	v_and_b32_e32 v112, 0xffff0000, v112
	v_mul_f32_e32 v117, v216, v112
	v_lshlrev_b32_e32 v112, 16, v113
	v_mul_f32_e32 v118, v216, v112
	v_and_b32_e32 v112, 0xffff0000, v113
	v_mul_f32_e32 v116, v216, v116
	v_mul_f32_e32 v113, v216, v112
	v_mov_b32_e32 v112, 0
	v_cvt_pk_fp8_f32 v112, v116, v117
	v_cvt_pk_fp8_f32 v112, v118, v113 op_sel:[0,0,1]
	v_lshlrev_b32_e32 v113, 16, v114
	v_mul_f32_e32 v116, v216, v113
	v_and_b32_e32 v113, 0xffff0000, v114
	v_mul_f32_e32 v114, v216, v113
	v_lshlrev_b32_e32 v113, 16, v115
	v_mul_f32_e32 v117, v216, v113
	v_and_b32_e32 v113, 0xffff0000, v115
	v_mul_f32_e32 v115, v216, v113
	v_mov_b32_e32 v113, 0
	v_cvt_pk_fp8_f32 v113, v116, v114
	v_cvt_pk_fp8_f32 v113, v117, v115 op_sel:[0,0,1]
	global_store_dwordx2 v[218:219], v[112:113], off offset:672
	v_lshlrev_b32_e32 v112, 16, v108
	v_and_b32_e32 v108, 0xffff0000, v108
	v_mul_f32_e32 v113, v216, v108
	v_lshlrev_b32_e32 v108, 16, v109
	v_mul_f32_e32 v114, v216, v108
	v_and_b32_e32 v108, 0xffff0000, v109
	v_mul_f32_e32 v112, v216, v112
	v_mul_f32_e32 v109, v216, v108
	v_mov_b32_e32 v108, 0
	v_cvt_pk_fp8_f32 v108, v112, v113
	v_cvt_pk_fp8_f32 v108, v114, v109 op_sel:[0,0,1]
	v_lshlrev_b32_e32 v109, 16, v110
	v_mul_f32_e32 v112, v216, v109
	v_and_b32_e32 v109, 0xffff0000, v110
	v_mul_f32_e32 v110, v216, v109
	v_lshlrev_b32_e32 v109, 16, v111
	v_mul_f32_e32 v113, v216, v109
	v_and_b32_e32 v109, 0xffff0000, v111
	v_mul_f32_e32 v111, v216, v109
	v_mov_b32_e32 v109, 0
	v_cvt_pk_fp8_f32 v109, v112, v110
	v_cvt_pk_fp8_f32 v109, v113, v111 op_sel:[0,0,1]
	global_store_dwordx2 v[218:219], v[108:109], off offset:704
	v_lshlrev_b32_e32 v108, 16, v100
	v_and_b32_e32 v100, 0xffff0000, v100
	v_mul_f32_e32 v109, v216, v100
	v_lshlrev_b32_e32 v100, 16, v101
	v_mul_f32_e32 v110, v216, v100
	v_and_b32_e32 v100, 0xffff0000, v101
	v_mul_f32_e32 v108, v216, v108
	v_mul_f32_e32 v101, v216, v100
	v_mov_b32_e32 v100, 0
	v_cvt_pk_fp8_f32 v100, v108, v109
	v_cvt_pk_fp8_f32 v100, v110, v101 op_sel:[0,0,1]
	v_lshlrev_b32_e32 v101, 16, v102
	v_mul_f32_e32 v108, v216, v101
	v_and_b32_e32 v101, 0xffff0000, v102
	v_mul_f32_e32 v102, v216, v101
	v_lshlrev_b32_e32 v101, 16, v103
	v_mul_f32_e32 v109, v216, v101
	v_and_b32_e32 v101, 0xffff0000, v103
	v_mul_f32_e32 v103, v216, v101
	v_mov_b32_e32 v101, 0
	v_cvt_pk_fp8_f32 v101, v108, v102
	v_cvt_pk_fp8_f32 v101, v109, v103 op_sel:[0,0,1]
	global_store_dwordx2 v[218:219], v[100:101], off offset:736
	v_lshlrev_b32_e32 v100, 16, v28
	v_mul_f32_e32 v101, v216, v100
	v_and_b32_e32 v100, 0xffff0000, v28
	v_mul_f32_e32 v102, v216, v100
	v_lshlrev_b32_e32 v100, 16, v29
	v_mul_f32_e32 v103, v216, v100
	v_and_b32_e32 v100, 0xffff0000, v29
	v_mul_f32_e32 v108, v216, v100
	v_mov_b32_e32 v100, 0
	v_cvt_pk_fp8_f32 v100, v101, v102
	v_lshlrev_b32_e32 v101, 16, v30
	v_mul_f32_e32 v102, v216, v101
	v_and_b32_e32 v101, 0xffff0000, v30
	v_cvt_pk_fp8_f32 v100, v103, v108 op_sel:[0,0,1]
	v_mul_f32_e32 v103, v216, v101
	v_lshlrev_b32_e32 v101, 16, v31
	v_mul_f32_e32 v108, v216, v101
	v_and_b32_e32 v101, 0xffff0000, v31
	v_mul_f32_e32 v109, v216, v101
	v_mov_b32_e32 v101, 0
	v_cvt_pk_fp8_f32 v101, v102, v103
	s_waitcnt vmcnt(38)
	v_mfma_f32_16x16x32_bf16 v[28:31], v[96:99], v[28:31], v[64:67]
	v_cvt_pk_fp8_f32 v101, v108, v109 op_sel:[0,0,1]
	s_waitcnt vmcnt(37)
	v_mfma_f32_16x16x32_bf16 v[64:67], v[92:95], v[24:27], v[72:75]
	global_store_dwordx2 v[218:219], v[100:101], off offset:768
	v_lshlrev_b32_e32 v100, 16, v24
	v_mul_f32_e32 v101, v216, v100
	v_and_b32_e32 v100, 0xffff0000, v24
	v_mul_f32_e32 v102, v216, v100
	v_lshlrev_b32_e32 v100, 16, v25
	v_mul_f32_e32 v103, v216, v100
	v_and_b32_e32 v100, 0xffff0000, v25
	v_mul_f32_e32 v108, v216, v100
	v_mov_b32_e32 v100, 0
	v_cvt_pk_fp8_f32 v100, v101, v102
	v_lshlrev_b32_e32 v101, 16, v26
	v_mul_f32_e32 v102, v216, v101
	v_and_b32_e32 v101, 0xffff0000, v26
	v_cvt_pk_fp8_f32 v100, v103, v108 op_sel:[0,0,1]
	v_mul_f32_e32 v103, v216, v101
	v_lshlrev_b32_e32 v101, 16, v27
	v_mul_f32_e32 v108, v216, v101
	v_and_b32_e32 v101, 0xffff0000, v27
	v_mul_f32_e32 v109, v216, v101
	v_mov_b32_e32 v101, 0
	v_cvt_pk_fp8_f32 v101, v102, v103
	s_waitcnt vmcnt(37)
	v_mfma_f32_16x16x32_bf16 v[24:27], v[88:91], v[24:27], v[28:31]
	v_cvt_pk_fp8_f32 v101, v108, v109 op_sel:[0,0,1]
	s_waitcnt vmcnt(36)
	v_mfma_f32_16x16x32_bf16 v[28:31], v[84:87], v[20:23], v[64:67]
	global_store_dwordx2 v[218:219], v[100:101], off offset:800
	v_lshlrev_b32_e32 v100, 16, v20
	v_mul_f32_e32 v101, v216, v100
	v_and_b32_e32 v100, 0xffff0000, v20
	v_mul_f32_e32 v102, v216, v100
	v_lshlrev_b32_e32 v100, 16, v21
	v_mul_f32_e32 v103, v216, v100
	v_and_b32_e32 v100, 0xffff0000, v21
	v_mul_f32_e32 v108, v216, v100
	v_mov_b32_e32 v100, 0
	v_cvt_pk_fp8_f32 v100, v101, v102
	v_lshlrev_b32_e32 v101, 16, v22
	v_mul_f32_e32 v102, v216, v101
	v_and_b32_e32 v101, 0xffff0000, v22
	v_cvt_pk_fp8_f32 v100, v103, v108 op_sel:[0,0,1]
	v_mul_f32_e32 v103, v216, v101
	v_lshlrev_b32_e32 v101, 16, v23
	v_mul_f32_e32 v108, v216, v101
	v_and_b32_e32 v101, 0xffff0000, v23
	v_mul_f32_e32 v109, v216, v101
	v_mov_b32_e32 v101, 0
	v_cvt_pk_fp8_f32 v101, v102, v103
	s_waitcnt vmcnt(36)
	v_mfma_f32_16x16x32_bf16 v[20:23], v[80:83], v[20:23], v[24:27]
	v_cvt_pk_fp8_f32 v101, v108, v109 op_sel:[0,0,1]
	s_waitcnt vmcnt(35)
	v_mfma_f32_16x16x32_bf16 v[24:27], v[76:79], v[16:19], v[28:31]
	global_store_dwordx2 v[218:219], v[100:101], off offset:832
	v_lshlrev_b32_e32 v100, 16, v16
	v_mul_f32_e32 v101, v216, v100
	v_and_b32_e32 v100, 0xffff0000, v16
	v_mul_f32_e32 v102, v216, v100
	v_lshlrev_b32_e32 v100, 16, v17
	v_mul_f32_e32 v103, v216, v100
	v_and_b32_e32 v100, 0xffff0000, v17
	v_mul_f32_e32 v108, v216, v100
	v_mov_b32_e32 v100, 0
	v_cvt_pk_fp8_f32 v100, v101, v102
	v_lshlrev_b32_e32 v101, 16, v18
	v_mul_f32_e32 v102, v216, v101
	v_and_b32_e32 v101, 0xffff0000, v18
	v_cvt_pk_fp8_f32 v100, v103, v108 op_sel:[0,0,1]
	v_mul_f32_e32 v103, v216, v101
	v_lshlrev_b32_e32 v101, 16, v19
	v_mul_f32_e32 v108, v216, v101
	v_and_b32_e32 v101, 0xffff0000, v19
	v_mul_f32_e32 v109, v216, v101
	v_mov_b32_e32 v101, 0
	v_cvt_pk_fp8_f32 v101, v102, v103
	s_waitcnt vmcnt(35)
	v_mfma_f32_16x16x32_bf16 v[16:19], v[68:71], v[16:19], v[20:23]
	v_cvt_pk_fp8_f32 v101, v108, v109 op_sel:[0,0,1]
	s_waitcnt vmcnt(34)
	v_mfma_f32_16x16x32_bf16 v[20:23], v[60:63], v[12:15], v[24:27]
	global_store_dwordx2 v[218:219], v[100:101], off offset:864
	v_lshlrev_b32_e32 v100, 16, v12
	v_mul_f32_e32 v101, v216, v100
	v_and_b32_e32 v100, 0xffff0000, v12
	v_mul_f32_e32 v102, v216, v100
	v_lshlrev_b32_e32 v100, 16, v13
	v_mul_f32_e32 v103, v216, v100
	v_and_b32_e32 v100, 0xffff0000, v13
	v_mul_f32_e32 v108, v216, v100
	v_mov_b32_e32 v100, 0
	v_cvt_pk_fp8_f32 v100, v101, v102
	v_lshlrev_b32_e32 v101, 16, v14
	v_mul_f32_e32 v102, v216, v101
	v_and_b32_e32 v101, 0xffff0000, v14
	v_cvt_pk_fp8_f32 v100, v103, v108 op_sel:[0,0,1]
	v_mul_f32_e32 v103, v216, v101
	v_lshlrev_b32_e32 v101, 16, v15
	v_mul_f32_e32 v108, v216, v101
	v_and_b32_e32 v101, 0xffff0000, v15
	v_mul_f32_e32 v109, v216, v101
	v_mov_b32_e32 v101, 0
	v_cvt_pk_fp8_f32 v101, v102, v103
	s_waitcnt vmcnt(34)
	v_mfma_f32_16x16x32_bf16 v[12:15], v[56:59], v[12:15], v[16:19]
	v_mov_b32_e32 v26, 0
	v_cvt_pk_fp8_f32 v101, v108, v109 op_sel:[0,0,1]
	s_waitcnt vmcnt(33)
	v_mfma_f32_16x16x32_bf16 v[16:19], v[52:55], v[8:11], v[20:23]
	global_store_dwordx2 v[218:219], v[100:101], off offset:896
	v_lshlrev_b32_e32 v100, 16, v8
	v_mul_f32_e32 v101, v216, v100
	v_and_b32_e32 v100, 0xffff0000, v8
	v_mul_f32_e32 v102, v216, v100
	v_lshlrev_b32_e32 v100, 16, v9
	v_mul_f32_e32 v103, v216, v100
	v_and_b32_e32 v100, 0xffff0000, v9
	v_mul_f32_e32 v108, v216, v100
	v_mov_b32_e32 v100, 0
	v_cvt_pk_fp8_f32 v100, v101, v102
	v_lshlrev_b32_e32 v101, 16, v10
	v_mul_f32_e32 v102, v216, v101
	v_and_b32_e32 v101, 0xffff0000, v10
	v_cvt_pk_fp8_f32 v100, v103, v108 op_sel:[0,0,1]
	v_mul_f32_e32 v103, v216, v101
	v_lshlrev_b32_e32 v101, 16, v11
	v_mul_f32_e32 v108, v216, v101
	v_and_b32_e32 v101, 0xffff0000, v11
	v_mul_f32_e32 v109, v216, v101
	v_mov_b32_e32 v101, 0
	v_cvt_pk_fp8_f32 v101, v102, v103
	s_waitcnt vmcnt(33)
	v_mfma_f32_16x16x32_bf16 v[8:11], v[48:51], v[8:11], v[12:15]
	v_cvt_pk_fp8_f32 v101, v108, v109 op_sel:[0,0,1]
	s_waitcnt vmcnt(32)
	v_mfma_f32_16x16x32_bf16 v[12:15], v[44:47], v[4:7], v[16:19]
	global_store_dwordx2 v[218:219], v[100:101], off offset:928
	v_lshlrev_b32_e32 v100, 16, v4
	v_mul_f32_e32 v101, v216, v100
	v_and_b32_e32 v100, 0xffff0000, v4
	v_mul_f32_e32 v102, v216, v100
	v_lshlrev_b32_e32 v100, 16, v5
	v_mul_f32_e32 v103, v216, v100
	v_and_b32_e32 v100, 0xffff0000, v5
	v_mul_f32_e32 v108, v216, v100
	v_mov_b32_e32 v100, 0
	v_cvt_pk_fp8_f32 v100, v101, v102
	v_lshlrev_b32_e32 v101, 16, v6
	v_mul_f32_e32 v102, v216, v101
	v_and_b32_e32 v101, 0xffff0000, v6
	v_cvt_pk_fp8_f32 v100, v103, v108 op_sel:[0,0,1]
	v_mul_f32_e32 v103, v216, v101
	v_lshlrev_b32_e32 v101, 16, v7
	v_mul_f32_e32 v108, v216, v101
	v_and_b32_e32 v101, 0xffff0000, v7
	v_mul_f32_e32 v109, v216, v101
	v_mov_b32_e32 v101, 0
	v_cvt_pk_fp8_f32 v101, v102, v103
	s_waitcnt vmcnt(32)
	v_mfma_f32_16x16x32_bf16 v[4:7], v[32:35], v[4:7], v[8:11]
	v_mov_b32_e32 v34, 0
	v_cvt_pk_fp8_f32 v101, v108, v109 op_sel:[0,0,1]
	s_waitcnt vmcnt(31)
	v_mfma_f32_16x16x32_bf16 v[8:11], v[36:39], v[0:3], v[12:15]
	global_store_dwordx2 v[218:219], v[100:101], off offset:960
	v_lshlrev_b32_e32 v100, 16, v0
	v_mul_f32_e32 v101, v216, v100
	v_and_b32_e32 v100, 0xffff0000, v0
	v_mul_f32_e32 v102, v216, v100
	v_lshlrev_b32_e32 v100, 16, v1
	v_mul_f32_e32 v103, v216, v100
	v_and_b32_e32 v100, 0xffff0000, v1
	v_mul_f32_e32 v108, v216, v100
	v_mov_b32_e32 v100, 0
	v_cvt_pk_fp8_f32 v100, v101, v102
	v_lshlrev_b32_e32 v101, 16, v2
	v_mul_f32_e32 v102, v216, v101
	v_and_b32_e32 v101, 0xffff0000, v2
	v_cvt_pk_fp8_f32 v100, v103, v108 op_sel:[0,0,1]
	v_mul_f32_e32 v103, v216, v101
	v_lshlrev_b32_e32 v101, 16, v3
	v_mul_f32_e32 v108, v216, v101
	v_and_b32_e32 v101, 0xffff0000, v3
	v_mul_f32_e32 v109, v216, v101
	v_mov_b32_e32 v101, 0
	v_cvt_pk_fp8_f32 v101, v102, v103
	s_waitcnt vmcnt(31)
	v_mfma_f32_16x16x32_bf16 v[0:3], v[40:43], v[0:3], v[4:7]
	v_cvt_pk_fp8_f32 v101, v108, v109 op_sel:[0,0,1]
	global_store_dwordx2 v[218:219], v[100:101], off offset:992
	s_nop 7
	s_nop 3
	v_pk_fma_f32 v[4:5], v[216:217], v[8:9], v[232:233] op_sel_hi:[0,1,1]
	v_pk_fma_f32 v[0:1], v[216:217], v[0:1], v[236:237] op_sel_hi:[0,1,1]
	ds_write2_b32 v221, v0, v1 offset0:16 offset1:17
	v_pk_fma_f32 v[0:1], v[216:217], v[10:11], v[234:235] op_sel_hi:[0,1,1]
	ds_write2_b32 v221, v0, v1 offset0:2 offset1:3
	v_pk_fma_f32 v[0:1], v[216:217], v[2:3], v[238:239] op_sel_hi:[0,1,1]
	ds_write2_b32 v221, v4, v5 offset1:1
	ds_write2_b32 v221, v0, v1 offset0:18 offset1:19
	s_waitcnt lgkmcnt(0)
	v_mov_b32_e32 v3, 0
	v_mov_b32_e32 v2, 0
	v_mov_b32_e32 v4, 0
	v_mov_b32_e32 v5, 0
	v_mov_b32_e32 v6, 0
	v_mov_b32_e32 v1, 0
	v_mov_b32_e32 v0, 0
	s_and_saveexec_b64 s[30:31], s[4:5]
	s_cbranch_execz .LBB0_1413
	ds_read2_b32 v[34:35], v224 offset1:1
	ds_read2_b32 v[32:33], v224 offset0:2 offset1:3
	ds_read2_b32 v[30:31], v224 offset0:4 offset1:5
	ds_read2_b32 v[28:29], v224 offset0:6 offset1:7
	ds_read2_b32 v[24:25], v224 offset0:8 offset1:9
	ds_read2_b32 v[22:23], v224 offset0:10 offset1:11
	ds_read2_b32 v[20:21], v224 offset0:12 offset1:13
	ds_read2_b32 v[18:19], v224 offset0:14 offset1:15
	ds_read2_b32 v[16:17], v224 offset0:16 offset1:17
	ds_read2_b32 v[14:15], v224 offset0:18 offset1:19
	ds_read2_b32 v[12:13], v224 offset0:20 offset1:21
	ds_read2_b32 v[10:11], v224 offset0:22 offset1:23
	ds_read2_b32 v[8:9], v224 offset0:24 offset1:25
	ds_read2_b32 v[6:7], v224 offset0:26 offset1:27
	ds_read2_b32 v[4:5], v224 offset0:28 offset1:29
	ds_read2_b32 v[2:3], v224 offset0:30 offset1:31
	s_waitcnt lgkmcnt(14)
	v_cmp_gt_f32_e32 vcc, v35, v34
	s_nop 1
	v_cndmask_b32_e32 v0, v34, v35, vcc
	v_cndmask_b32_e64 v1, 0, 1, vcc
	v_cmp_gt_f32_e32 vcc, v32, v0
	s_nop 1
	v_cndmask_b32_e32 v0, v0, v32, vcc
	v_cndmask_b32_e64 v1, v1, 2, vcc
	v_cmp_gt_f32_e32 vcc, v33, v0
	s_nop 1
	v_cndmask_b32_e32 v0, v0, v33, vcc
	v_cndmask_b32_e64 v1, v1, 3, vcc
	s_waitcnt lgkmcnt(13)
	v_cmp_gt_f32_e32 vcc, v30, v0
	s_nop 1
	v_cndmask_b32_e32 v0, v0, v30, vcc
	v_cndmask_b32_e64 v1, v1, 4, vcc
	v_cmp_gt_f32_e32 vcc, v31, v0
	s_nop 1
	v_cndmask_b32_e32 v0, v0, v31, vcc
	v_cndmask_b32_e64 v1, v1, 5, vcc
	s_waitcnt lgkmcnt(12)
	v_cmp_gt_f32_e32 vcc, v28, v0
	s_nop 1
	v_cndmask_b32_e32 v0, v0, v28, vcc
	v_cndmask_b32_e64 v1, v1, 6, vcc
	v_cmp_gt_f32_e32 vcc, v29, v0
	s_nop 1
	v_cndmask_b32_e32 v0, v0, v29, vcc
	v_cndmask_b32_e64 v1, v1, 7, vcc
	s_waitcnt lgkmcnt(11)
	v_cmp_gt_f32_e32 vcc, v24, v0
	s_nop 1
	v_cndmask_b32_e32 v0, v0, v24, vcc
	v_cndmask_b32_e64 v1, v1, 8, vcc
	v_cmp_gt_f32_e32 vcc, v25, v0
	s_nop 1
	v_cndmask_b32_e32 v0, v0, v25, vcc
	v_cndmask_b32_e64 v1, v1, 9, vcc
	s_waitcnt lgkmcnt(10)
	v_cmp_gt_f32_e32 vcc, v22, v0
	s_nop 1
	v_cndmask_b32_e32 v0, v0, v22, vcc
	v_cndmask_b32_e64 v1, v1, 10, vcc
	v_cmp_gt_f32_e32 vcc, v23, v0
	s_nop 1
	v_cndmask_b32_e32 v0, v0, v23, vcc
	v_cndmask_b32_e64 v1, v1, 11, vcc
	s_waitcnt lgkmcnt(9)
	v_cmp_gt_f32_e32 vcc, v20, v0
	s_nop 1
	v_cndmask_b32_e32 v0, v0, v20, vcc
	v_cndmask_b32_e64 v1, v1, 12, vcc
	v_cmp_gt_f32_e32 vcc, v21, v0
	s_nop 1
	v_cndmask_b32_e32 v0, v0, v21, vcc
	v_cndmask_b32_e64 v1, v1, 13, vcc
	s_waitcnt lgkmcnt(8)
	v_cmp_gt_f32_e32 vcc, v18, v0
	s_nop 1
	v_cndmask_b32_e32 v0, v0, v18, vcc
	v_cndmask_b32_e64 v1, v1, 14, vcc
	v_cmp_gt_f32_e32 vcc, v19, v0
	s_nop 1
	v_cndmask_b32_e32 v0, v0, v19, vcc
	v_cndmask_b32_e64 v1, v1, 15, vcc
	s_waitcnt lgkmcnt(7)
	v_cmp_gt_f32_e32 vcc, v16, v0
	s_nop 1
	v_cndmask_b32_e32 v0, v0, v16, vcc
	v_cndmask_b32_e64 v1, v1, 16, vcc
	v_cmp_gt_f32_e32 vcc, v17, v0
	s_nop 1
	v_cndmask_b32_e32 v0, v0, v17, vcc
	v_cndmask_b32_e64 v1, v1, 17, vcc
	s_waitcnt lgkmcnt(6)
	v_cmp_gt_f32_e32 vcc, v14, v0
	s_nop 1
	v_cndmask_b32_e32 v0, v0, v14, vcc
	v_cndmask_b32_e64 v1, v1, 18, vcc
	v_cmp_gt_f32_e32 vcc, v15, v0
	s_nop 1
	v_cndmask_b32_e32 v0, v0, v15, vcc
	v_cndmask_b32_e64 v1, v1, 19, vcc
	s_waitcnt lgkmcnt(5)
	v_cmp_gt_f32_e32 vcc, v12, v0
	s_nop 1
	v_cndmask_b32_e32 v0, v0, v12, vcc
	v_cndmask_b32_e64 v1, v1, 20, vcc
	v_cmp_gt_f32_e32 vcc, v13, v0
	s_nop 1
	v_cndmask_b32_e32 v0, v0, v13, vcc
	v_cndmask_b32_e64 v1, v1, 21, vcc
	s_waitcnt lgkmcnt(4)
	v_cmp_gt_f32_e32 vcc, v10, v0
	s_nop 1
	v_cndmask_b32_e32 v0, v0, v10, vcc
	v_cndmask_b32_e64 v1, v1, 22, vcc
	v_cmp_gt_f32_e32 vcc, v11, v0
	s_nop 1
	v_cndmask_b32_e32 v0, v0, v11, vcc
	v_cndmask_b32_e64 v1, v1, 23, vcc
	s_waitcnt lgkmcnt(3)
	v_cmp_gt_f32_e32 vcc, v8, v0
	s_nop 1
	v_cndmask_b32_e32 v0, v0, v8, vcc
	v_cndmask_b32_e64 v1, v1, 24, vcc
	v_cmp_gt_f32_e32 vcc, v9, v0
	s_nop 1
	v_cndmask_b32_e32 v0, v0, v9, vcc
	v_cndmask_b32_e64 v1, v1, 25, vcc
	s_waitcnt lgkmcnt(2)
	v_cmp_gt_f32_e32 vcc, v6, v0
	s_nop 1
	v_cndmask_b32_e32 v0, v0, v6, vcc
	v_cndmask_b32_e64 v1, v1, 26, vcc
	v_cmp_gt_f32_e32 vcc, v7, v0
	s_nop 1
	v_cndmask_b32_e32 v0, v0, v7, vcc
	v_cndmask_b32_e64 v1, v1, 27, vcc
	s_waitcnt lgkmcnt(1)
	v_cmp_gt_f32_e32 vcc, v4, v0
	s_nop 1
	v_cndmask_b32_e32 v0, v0, v4, vcc
	v_cndmask_b32_e64 v1, v1, 28, vcc
	v_cmp_gt_f32_e32 vcc, v5, v0
	s_nop 1
	v_cndmask_b32_e32 v0, v0, v5, vcc
	v_cndmask_b32_e64 v26, v1, 29, vcc
	s_waitcnt lgkmcnt(0)
	v_cmp_gt_f32_e32 vcc, v2, v0
	s_nop 1
	v_cndmask_b32_e32 v1, v0, v2, vcc
	v_cndmask_b32_e64 v0, v26, 30, vcc
	v_cmp_gt_f32_e32 vcc, v3, v1
	s_nop 1
	v_cndmask_b32_e64 v200, v0, 31, vcc
	v_cmp_eq_u32_e64 s[8:9], 0, v200
	v_lshlrev_b32_e64 v38, v200, 1
	v_and_b32_e32 v27, 2, v38
	v_cndmask_b32_e64 v0, v34, 0, s[8:9]
	v_cmp_gt_f32_e64 s[10:11], v35, v0
	v_cndmask_b32_e64 v26, 0, -1, s[8:9]
	s_or_b64 s[8:9], s[8:9], s[10:11]
	v_cndmask_b32_e64 v36, v34, v35, s[8:9]
	v_cndmask_b32_e64 v37, 0, 1, s[8:9]
	v_cmp_eq_u32_e64 s[8:9], 0, v27
	v_and_b32_e32 v27, 4, v38
	s_nop 0
	v_cndmask_b32_e64 v0, v0, v36, s[8:9]
	v_cndmask_b32_e64 v26, v26, v37, s[8:9]
	v_cmp_eq_u32_e64 s[8:9], 0, v27
	v_cmp_gt_f32_e64 s[10:11], v32, v0
	s_and_b64 s[8:9], s[8:9], s[10:11]
	v_cndmask_b32_e64 v27, v0, v32, s[8:9]
	v_cndmask_b32_e64 v0, v26, 2, s[8:9]
	v_and_b32_e32 v26, 8, v38
	v_cmp_eq_u32_e64 s[8:9], 0, v26
	s_and_saveexec_b64 s[48:49], s[8:9]
	v_cmp_gt_i32_e64 s[8:9], 0, v0
	v_cmp_gt_f32_e64 s[10:11], v33, v27
	s_or_b64 s[8:9], s[8:9], s[10:11]
	v_cndmask_b32_e64 v27, v27, v33, s[8:9]
	v_cndmask_b32_e64 v0, v0, 3, s[8:9]
	s_or_b64 exec, exec, s[48:49]
	v_and_b32_e32 v26, 16, v38
	v_cmp_eq_u32_e64 s[8:9], 0, v26
	s_and_saveexec_b64 s[48:49], s[8:9]
	v_cmp_gt_i32_e64 s[8:9], 0, v0
	v_cmp_gt_f32_e64 s[10:11], v30, v27
	s_or_b64 s[8:9], s[8:9], s[10:11]
	v_cndmask_b32_e64 v27, v27, v30, s[8:9]
	v_cndmask_b32_e64 v0, v0, 4, s[8:9]
	s_or_b64 exec, exec, s[48:49]
	v_and_b32_e32 v26, 32, v38
	v_cmp_eq_u32_e64 s[8:9], 0, v26
	s_and_saveexec_b64 s[48:49], s[8:9]
	v_cmp_gt_i32_e64 s[8:9], 0, v0
	v_cmp_gt_f32_e64 s[10:11], v31, v27
	s_or_b64 s[8:9], s[8:9], s[10:11]
	v_cndmask_b32_e64 v27, v27, v31, s[8:9]
	v_cndmask_b32_e64 v0, v0, 5, s[8:9]
	s_or_b64 exec, exec, s[48:49]
	v_and_b32_e32 v26, 64, v38
	v_cmp_eq_u32_e64 s[8:9], 0, v26
	s_and_saveexec_b64 s[48:49], s[8:9]
	v_cmp_gt_i32_e64 s[8:9], 0, v0
	v_cmp_gt_f32_e64 s[10:11], v28, v27
	s_or_b64 s[8:9], s[8:9], s[10:11]
	v_cndmask_b32_e64 v27, v27, v28, s[8:9]
	v_cndmask_b32_e64 v0, v0, 6, s[8:9]
	s_or_b64 exec, exec, s[48:49]
	v_and_b32_e32 v26, 0x80, v38
	v_cmp_eq_u32_e64 s[8:9], 0, v26
	s_and_saveexec_b64 s[48:49], s[8:9]
	v_cmp_gt_i32_e64 s[8:9], 0, v0
	v_cmp_gt_f32_e64 s[10:11], v29, v27
	s_or_b64 s[8:9], s[8:9], s[10:11]
	v_cndmask_b32_e64 v27, v27, v29, s[8:9]
	v_cndmask_b32_e64 v0, v0, 7, s[8:9]
	s_or_b64 exec, exec, s[48:49]
	v_and_b32_e32 v26, 0x100, v38
	v_cmp_eq_u32_e64 s[8:9], 0, v26
	s_and_saveexec_b64 s[48:49], s[8:9]
	v_cmp_gt_i32_e64 s[8:9], 0, v0
	v_cmp_gt_f32_e64 s[10:11], v24, v27
	s_or_b64 s[8:9], s[8:9], s[10:11]
	v_cndmask_b32_e64 v27, v27, v24, s[8:9]
	v_cndmask_b32_e64 v0, v0, 8, s[8:9]
	s_or_b64 exec, exec, s[48:49]
	v_and_b32_e32 v26, 0x200, v38
	v_cmp_eq_u32_e64 s[8:9], 0, v26
	s_and_saveexec_b64 s[48:49], s[8:9]
	v_cmp_gt_i32_e64 s[8:9], 0, v0
	v_cmp_gt_f32_e64 s[10:11], v25, v27
	s_or_b64 s[8:9], s[8:9], s[10:11]
	v_cndmask_b32_e64 v27, v27, v25, s[8:9]
	v_cndmask_b32_e64 v0, v0, 9, s[8:9]
	s_or_b64 exec, exec, s[48:49]
	v_and_b32_e32 v26, 0x400, v38
	v_cmp_eq_u32_e64 s[8:9], 0, v26
	s_and_saveexec_b64 s[48:49], s[8:9]
	v_cmp_gt_i32_e64 s[8:9], 0, v0
	v_cmp_gt_f32_e64 s[10:11], v22, v27
	s_or_b64 s[8:9], s[8:9], s[10:11]
	v_cndmask_b32_e64 v27, v27, v22, s[8:9]
	v_cndmask_b32_e64 v0, v0, 10, s[8:9]
	s_or_b64 exec, exec, s[48:49]
	v_and_b32_e32 v26, 0x800, v38
	v_cmp_eq_u32_e64 s[8:9], 0, v26
	s_and_saveexec_b64 s[48:49], s[8:9]
	v_cmp_gt_i32_e64 s[8:9], 0, v0
	v_cmp_gt_f32_e64 s[10:11], v23, v27
	s_or_b64 s[8:9], s[8:9], s[10:11]
	v_cndmask_b32_e64 v27, v27, v23, s[8:9]
	v_cndmask_b32_e64 v0, v0, 11, s[8:9]
	s_or_b64 exec, exec, s[48:49]
	v_and_b32_e32 v26, 0x1000, v38
	v_cmp_eq_u32_e64 s[8:9], 0, v26
	s_and_saveexec_b64 s[48:49], s[8:9]
	v_cmp_gt_i32_e64 s[8:9], 0, v0
	v_cmp_gt_f32_e64 s[10:11], v20, v27
	s_or_b64 s[8:9], s[8:9], s[10:11]
	v_cndmask_b32_e64 v27, v27, v20, s[8:9]
	v_cndmask_b32_e64 v0, v0, 12, s[8:9]
	s_or_b64 exec, exec, s[48:49]
	v_and_b32_e32 v26, 0x2000, v38
	v_cmp_eq_u32_e64 s[8:9], 0, v26
	s_and_saveexec_b64 s[48:49], s[8:9]
	v_cmp_gt_i32_e64 s[8:9], 0, v0
	v_cmp_gt_f32_e64 s[10:11], v21, v27
	s_or_b64 s[8:9], s[8:9], s[10:11]
	v_cndmask_b32_e64 v27, v27, v21, s[8:9]
	v_cndmask_b32_e64 v0, v0, 13, s[8:9]
	s_or_b64 exec, exec, s[48:49]
	v_and_b32_e32 v26, 0x4000, v38
	v_cmp_eq_u32_e64 s[8:9], 0, v26
	s_and_saveexec_b64 s[48:49], s[8:9]
	v_cmp_gt_i32_e64 s[8:9], 0, v0
	v_cmp_gt_f32_e64 s[10:11], v18, v27
	s_or_b64 s[8:9], s[8:9], s[10:11]
	v_cndmask_b32_e64 v27, v27, v18, s[8:9]
	v_cndmask_b32_e64 v0, v0, 14, s[8:9]
	s_or_b64 exec, exec, s[48:49]
	v_and_b32_e32 v26, 0x8000, v38
	v_cmp_eq_u32_e64 s[8:9], 0, v26
	s_and_saveexec_b64 s[48:49], s[8:9]
	v_cmp_gt_i32_e64 s[8:9], 0, v0
	v_cmp_gt_f32_e64 s[10:11], v19, v27
	s_or_b64 s[8:9], s[8:9], s[10:11]
	v_cndmask_b32_e64 v27, v27, v19, s[8:9]
	v_cndmask_b32_e64 v0, v0, 15, s[8:9]
	s_or_b64 exec, exec, s[48:49]
	v_and_b32_e32 v26, 0x10000, v38
	v_cmp_eq_u32_e64 s[8:9], 0, v26
	s_and_saveexec_b64 s[48:49], s[8:9]
	v_cmp_gt_i32_e64 s[8:9], 0, v0
	v_cmp_gt_f32_e64 s[10:11], v16, v27
	s_or_b64 s[8:9], s[8:9], s[10:11]
	v_cndmask_b32_e64 v27, v27, v16, s[8:9]
	v_cndmask_b32_e64 v0, v0, 16, s[8:9]
	s_or_b64 exec, exec, s[48:49]
	v_and_b32_e32 v26, 0x20000, v38
	v_cmp_eq_u32_e64 s[8:9], 0, v26
	s_and_saveexec_b64 s[48:49], s[8:9]
	v_cmp_gt_i32_e64 s[8:9], 0, v0
	v_cmp_gt_f32_e64 s[10:11], v17, v27
	s_or_b64 s[8:9], s[8:9], s[10:11]
	v_cndmask_b32_e64 v27, v27, v17, s[8:9]
	v_cndmask_b32_e64 v0, v0, 17, s[8:9]
	s_or_b64 exec, exec, s[48:49]
	v_and_b32_e32 v26, 0x40000, v38
	v_cmp_eq_u32_e64 s[8:9], 0, v26
	s_and_saveexec_b64 s[48:49], s[8:9]
	v_cmp_gt_i32_e64 s[8:9], 0, v0
	v_cmp_gt_f32_e64 s[10:11], v14, v27
	s_or_b64 s[8:9], s[8:9], s[10:11]
	v_cndmask_b32_e64 v27, v27, v14, s[8:9]
	v_cndmask_b32_e64 v0, v0, 18, s[8:9]
	s_or_b64 exec, exec, s[48:49]
	v_and_b32_e32 v26, 0x80000, v38
	v_cmp_eq_u32_e64 s[8:9], 0, v26
	s_and_saveexec_b64 s[48:49], s[8:9]
	v_cmp_gt_i32_e64 s[8:9], 0, v0
	v_cmp_gt_f32_e64 s[10:11], v15, v27
	s_or_b64 s[8:9], s[8:9], s[10:11]
	v_cndmask_b32_e64 v27, v27, v15, s[8:9]
	v_cndmask_b32_e64 v0, v0, 19, s[8:9]
	s_or_b64 exec, exec, s[48:49]
	v_and_b32_e32 v26, 0x100000, v38
	v_cmp_eq_u32_e64 s[8:9], 0, v26
	s_and_saveexec_b64 s[48:49], s[8:9]
	v_cmp_gt_i32_e64 s[8:9], 0, v0
	v_cmp_gt_f32_e64 s[10:11], v12, v27
	s_or_b64 s[8:9], s[8:9], s[10:11]
	v_cndmask_b32_e64 v27, v27, v12, s[8:9]
	v_cndmask_b32_e64 v0, v0, 20, s[8:9]
	s_or_b64 exec, exec, s[48:49]
	v_and_b32_e32 v26, 0x200000, v38
	v_cmp_eq_u32_e64 s[8:9], 0, v26
	s_and_saveexec_b64 s[48:49], s[8:9]
	v_cmp_gt_i32_e64 s[8:9], 0, v0
	v_cmp_gt_f32_e64 s[10:11], v13, v27
	s_or_b64 s[8:9], s[8:9], s[10:11]
	v_cndmask_b32_e64 v27, v27, v13, s[8:9]
	v_cndmask_b32_e64 v0, v0, 21, s[8:9]
	s_or_b64 exec, exec, s[48:49]
	v_and_b32_e32 v26, 0x400000, v38
	v_cmp_eq_u32_e64 s[8:9], 0, v26
	s_and_saveexec_b64 s[48:49], s[8:9]
	v_cmp_gt_i32_e64 s[8:9], 0, v0
	v_cmp_gt_f32_e64 s[10:11], v10, v27
	s_or_b64 s[8:9], s[8:9], s[10:11]
	v_cndmask_b32_e64 v27, v27, v10, s[8:9]
	v_cndmask_b32_e64 v0, v0, 22, s[8:9]
	s_or_b64 exec, exec, s[48:49]
	v_and_b32_e32 v26, 0x800000, v38
	v_cmp_eq_u32_e64 s[8:9], 0, v26
	s_and_saveexec_b64 s[48:49], s[8:9]
	v_cmp_gt_i32_e64 s[8:9], 0, v0
	v_cmp_gt_f32_e64 s[10:11], v11, v27
	s_or_b64 s[8:9], s[8:9], s[10:11]
	v_cndmask_b32_e64 v27, v27, v11, s[8:9]
	v_cndmask_b32_e64 v0, v0, 23, s[8:9]
	s_or_b64 exec, exec, s[48:49]
	v_and_b32_e32 v26, 0x1000000, v38
	v_cmp_eq_u32_e64 s[8:9], 0, v26
	s_and_saveexec_b64 s[48:49], s[8:9]
	v_cmp_gt_i32_e64 s[8:9], 0, v0
	v_cmp_gt_f32_e64 s[10:11], v8, v27
	s_or_b64 s[8:9], s[8:9], s[10:11]
	v_cndmask_b32_e64 v27, v27, v8, s[8:9]
	v_cndmask_b32_e64 v0, v0, 24, s[8:9]
	s_or_b64 exec, exec, s[48:49]
	v_and_b32_e32 v26, 0x2000000, v38
	v_cmp_eq_u32_e64 s[8:9], 0, v26
	s_and_saveexec_b64 s[48:49], s[8:9]
	v_cmp_gt_i32_e64 s[8:9], 0, v0
	v_cmp_gt_f32_e64 s[10:11], v9, v27
	s_or_b64 s[8:9], s[8:9], s[10:11]
	v_cndmask_b32_e64 v27, v27, v9, s[8:9]
	v_cndmask_b32_e64 v0, v0, 25, s[8:9]
	s_or_b64 exec, exec, s[48:49]
	v_and_b32_e32 v26, 0x4000000, v38
	v_cmp_eq_u32_e64 s[8:9], 0, v26
	s_and_saveexec_b64 s[48:49], s[8:9]
	v_cmp_gt_i32_e64 s[8:9], 0, v0
	v_cmp_gt_f32_e64 s[10:11], v6, v27
	s_or_b64 s[8:9], s[8:9], s[10:11]
	v_cndmask_b32_e64 v27, v27, v6, s[8:9]
	v_cndmask_b32_e64 v0, v0, 26, s[8:9]
	s_or_b64 exec, exec, s[48:49]
	v_and_b32_e32 v26, 0x8000000, v38
	v_cmp_eq_u32_e64 s[8:9], 0, v26
	s_and_saveexec_b64 s[48:49], s[8:9]
	v_cmp_gt_i32_e64 s[8:9], 0, v0
	v_cmp_gt_f32_e64 s[10:11], v7, v27
	s_or_b64 s[8:9], s[8:9], s[10:11]
	v_cndmask_b32_e64 v27, v27, v7, s[8:9]
	v_cndmask_b32_e64 v0, v0, 27, s[8:9]
	s_or_b64 exec, exec, s[48:49]
	v_and_b32_e32 v26, 0x10000000, v38
	v_cmp_eq_u32_e64 s[8:9], 0, v26
	s_and_saveexec_b64 s[48:49], s[8:9]
	v_cmp_gt_i32_e64 s[8:9], 0, v0
	v_cmp_gt_f32_e64 s[10:11], v4, v27
	s_or_b64 s[8:9], s[8:9], s[10:11]
	v_cndmask_b32_e64 v27, v27, v4, s[8:9]
	v_cndmask_b32_e64 v0, v0, 28, s[8:9]
	s_or_b64 exec, exec, s[48:49]
	v_and_b32_e32 v26, 0x20000000, v38
	v_cmp_eq_u32_e64 s[8:9], 0, v26
	s_and_saveexec_b64 s[48:49], s[8:9]
	v_cmp_gt_i32_e64 s[8:9], 0, v0
	v_cmp_gt_f32_e64 s[10:11], v5, v27
	s_or_b64 s[8:9], s[8:9], s[10:11]
	v_cndmask_b32_e64 v27, v27, v5, s[8:9]
	v_cndmask_b32_e64 v0, v0, 29, s[8:9]
	s_or_b64 exec, exec, s[48:49]
	v_and_b32_e32 v26, 2.0, v38
	v_cmp_eq_u32_e64 s[8:9], 0, v26
	s_and_saveexec_b64 s[48:49], s[8:9]
	v_cmp_gt_i32_e64 s[8:9], 0, v0
	v_cmp_gt_f32_e64 s[10:11], v2, v27
	s_or_b64 s[8:9], s[8:9], s[10:11]
	v_cndmask_b32_e64 v27, v27, v2, s[8:9]
	v_cndmask_b32_e64 v0, v0, 30, s[8:9]
	s_or_b64 exec, exec, s[48:49]
	v_cmp_ne_u32_e64 s[8:9], 31, v200
	s_and_saveexec_b64 s[48:49], s[8:9]
	v_cmp_gt_i32_e64 s[8:9], 0, v0
	v_cmp_gt_f32_e64 s[10:11], v3, v27
	s_or_b64 s[8:9], s[8:9], s[10:11]
	v_cndmask_b32_e64 v27, v27, v3, s[8:9]
	v_cndmask_b32_e64 v0, v0, 31, s[8:9]
	s_or_b64 exec, exec, s[48:49]
	v_lshlrev_b32_e64 v39, v0, 1
	v_or_b32_e32 v37, v39, v38
	v_and_b32_e32 v26, 1, v37
	v_cmp_eq_u32_e64 s[8:9], 1, v26
	v_bitop3_b32 v36, v39, 2, v38 bitop3:0xc8
	v_bfe_i32 v40, v37, 0, 1
	v_cndmask_b32_e64 v26, v34, 0, s[8:9]
	v_cmp_gt_f32_e64 s[10:11], v35, v26
	s_or_b64 s[8:9], s[8:9], s[10:11]
	v_cndmask_b32_e64 v41, v34, v35, s[8:9]
	v_cndmask_b32_e64 v42, 0, 1, s[8:9]
	v_cmp_eq_u32_e64 s[8:9], 0, v36
	v_bitop3_b32 v38, v39, 4, v38 bitop3:0xc8
	s_nop 0
	v_cndmask_b32_e64 v36, v26, v41, s[8:9]
	v_cndmask_b32_e64 v26, v40, v42, s[8:9]
	v_cmp_eq_u32_e64 s[8:9], 0, v38
	s_and_saveexec_b64 s[48:49], s[8:9]
	v_and_b32_e32 v38, 3, v37
	v_cmp_eq_u32_e64 s[8:9], 3, v38
	v_cmp_gt_f32_e64 s[10:11], v32, v36
	s_or_b64 s[8:9], s[8:9], s[10:11]
	v_cndmask_b32_e64 v36, v36, v32, s[8:9]
	v_cndmask_b32_e64 v26, v26, 2, s[8:9]
	s_or_b64 exec, exec, s[48:49]
	v_and_b32_e32 v38, 8, v37
	v_cmp_eq_u32_e64 s[8:9], 0, v38
	s_and_saveexec_b64 s[48:49], s[8:9]
	v_cmp_gt_i32_e64 s[8:9], 0, v26
	v_cmp_gt_f32_e64 s[10:11], v33, v36
	s_or_b64 s[8:9], s[8:9], s[10:11]
	v_cndmask_b32_e64 v36, v36, v33, s[8:9]
	v_cndmask_b32_e64 v26, v26, 3, s[8:9]
	s_or_b64 exec, exec, s[48:49]
	v_and_b32_e32 v38, 16, v37
	v_cmp_eq_u32_e64 s[8:9], 0, v38
	s_and_saveexec_b64 s[48:49], s[8:9]
	v_cmp_gt_i32_e64 s[8:9], 0, v26
	v_cmp_gt_f32_e64 s[10:11], v30, v36
	s_or_b64 s[8:9], s[8:9], s[10:11]
	v_cndmask_b32_e64 v36, v36, v30, s[8:9]
	v_cndmask_b32_e64 v26, v26, 4, s[8:9]
	s_or_b64 exec, exec, s[48:49]
	v_and_b32_e32 v38, 32, v37
	v_cmp_eq_u32_e64 s[8:9], 0, v38
	s_and_saveexec_b64 s[48:49], s[8:9]
	v_cmp_gt_i32_e64 s[8:9], 0, v26
	v_cmp_gt_f32_e64 s[10:11], v31, v36
	s_or_b64 s[8:9], s[8:9], s[10:11]
	v_cndmask_b32_e64 v36, v36, v31, s[8:9]
	v_cndmask_b32_e64 v26, v26, 5, s[8:9]
	s_or_b64 exec, exec, s[48:49]
	v_and_b32_e32 v38, 64, v37
	v_cmp_eq_u32_e64 s[8:9], 0, v38
	s_and_saveexec_b64 s[48:49], s[8:9]
	v_cmp_gt_i32_e64 s[8:9], 0, v26
	v_cmp_gt_f32_e64 s[10:11], v28, v36
	s_or_b64 s[8:9], s[8:9], s[10:11]
	v_cndmask_b32_e64 v36, v36, v28, s[8:9]
	v_cndmask_b32_e64 v26, v26, 6, s[8:9]
	s_or_b64 exec, exec, s[48:49]
	v_and_b32_e32 v38, 0x80, v37
	v_cmp_eq_u32_e64 s[8:9], 0, v38
	s_and_saveexec_b64 s[48:49], s[8:9]
	v_cmp_gt_i32_e64 s[8:9], 0, v26
	v_cmp_gt_f32_e64 s[10:11], v29, v36
	s_or_b64 s[8:9], s[8:9], s[10:11]
	v_cndmask_b32_e64 v36, v36, v29, s[8:9]
	v_cndmask_b32_e64 v26, v26, 7, s[8:9]
	s_or_b64 exec, exec, s[48:49]
	v_and_b32_e32 v38, 0x100, v37
	v_cmp_eq_u32_e64 s[8:9], 0, v38
	s_and_saveexec_b64 s[48:49], s[8:9]
	v_cmp_gt_i32_e64 s[8:9], 0, v26
	v_cmp_gt_f32_e64 s[10:11], v24, v36
	s_or_b64 s[8:9], s[8:9], s[10:11]
	v_cndmask_b32_e64 v36, v36, v24, s[8:9]
	v_cndmask_b32_e64 v26, v26, 8, s[8:9]
	s_or_b64 exec, exec, s[48:49]
	v_and_b32_e32 v38, 0x200, v37
	v_cmp_eq_u32_e64 s[8:9], 0, v38
	s_and_saveexec_b64 s[48:49], s[8:9]
	v_cmp_gt_i32_e64 s[8:9], 0, v26
	v_cmp_gt_f32_e64 s[10:11], v25, v36
	s_or_b64 s[8:9], s[8:9], s[10:11]
	v_cndmask_b32_e64 v36, v36, v25, s[8:9]
	v_cndmask_b32_e64 v26, v26, 9, s[8:9]
	s_or_b64 exec, exec, s[48:49]
	v_and_b32_e32 v38, 0x400, v37
	v_cmp_eq_u32_e64 s[8:9], 0, v38
	s_and_saveexec_b64 s[48:49], s[8:9]
	v_cmp_gt_i32_e64 s[8:9], 0, v26
	v_cmp_gt_f32_e64 s[10:11], v22, v36
	s_or_b64 s[8:9], s[8:9], s[10:11]
	v_cndmask_b32_e64 v36, v36, v22, s[8:9]
	v_cndmask_b32_e64 v26, v26, 10, s[8:9]
	s_or_b64 exec, exec, s[48:49]
	v_and_b32_e32 v38, 0x800, v37
	v_cmp_eq_u32_e64 s[8:9], 0, v38
	s_and_saveexec_b64 s[48:49], s[8:9]
	v_cmp_gt_i32_e64 s[8:9], 0, v26
	v_cmp_gt_f32_e64 s[10:11], v23, v36
	s_or_b64 s[8:9], s[8:9], s[10:11]
	v_cndmask_b32_e64 v36, v36, v23, s[8:9]
	v_cndmask_b32_e64 v26, v26, 11, s[8:9]
	s_or_b64 exec, exec, s[48:49]
	v_and_b32_e32 v38, 0x1000, v37
	v_cmp_eq_u32_e64 s[8:9], 0, v38
	s_and_saveexec_b64 s[48:49], s[8:9]
	v_cmp_gt_i32_e64 s[8:9], 0, v26
	v_cmp_gt_f32_e64 s[10:11], v20, v36
	s_or_b64 s[8:9], s[8:9], s[10:11]
	v_cndmask_b32_e64 v36, v36, v20, s[8:9]
	v_cndmask_b32_e64 v26, v26, 12, s[8:9]
	s_or_b64 exec, exec, s[48:49]
	v_and_b32_e32 v38, 0x2000, v37
	v_cmp_eq_u32_e64 s[8:9], 0, v38
	s_and_saveexec_b64 s[48:49], s[8:9]
	v_cmp_gt_i32_e64 s[8:9], 0, v26
	v_cmp_gt_f32_e64 s[10:11], v21, v36
	s_or_b64 s[8:9], s[8:9], s[10:11]
	v_cndmask_b32_e64 v36, v36, v21, s[8:9]
	v_cndmask_b32_e64 v26, v26, 13, s[8:9]
	s_or_b64 exec, exec, s[48:49]
	v_and_b32_e32 v38, 0x4000, v37
	v_cmp_eq_u32_e64 s[8:9], 0, v38
	s_and_saveexec_b64 s[48:49], s[8:9]
	v_cmp_gt_i32_e64 s[8:9], 0, v26
	v_cmp_gt_f32_e64 s[10:11], v18, v36
	s_or_b64 s[8:9], s[8:9], s[10:11]
	v_cndmask_b32_e64 v36, v36, v18, s[8:9]
	v_cndmask_b32_e64 v26, v26, 14, s[8:9]
	s_or_b64 exec, exec, s[48:49]
	v_and_b32_e32 v38, 0x8000, v37
	v_cmp_eq_u32_e64 s[8:9], 0, v38
	s_and_saveexec_b64 s[48:49], s[8:9]
	v_cmp_gt_i32_e64 s[8:9], 0, v26
	v_cmp_gt_f32_e64 s[10:11], v19, v36
	s_or_b64 s[8:9], s[8:9], s[10:11]
	v_cndmask_b32_e64 v36, v36, v19, s[8:9]
	v_cndmask_b32_e64 v26, v26, 15, s[8:9]
	s_or_b64 exec, exec, s[48:49]
	v_and_b32_e32 v38, 0x10000, v37
	v_cmp_eq_u32_e64 s[8:9], 0, v38
	s_and_saveexec_b64 s[48:49], s[8:9]
	v_cmp_gt_i32_e64 s[8:9], 0, v26
	v_cmp_gt_f32_e64 s[10:11], v16, v36
	s_or_b64 s[8:9], s[8:9], s[10:11]
	v_cndmask_b32_e64 v36, v36, v16, s[8:9]
	v_cndmask_b32_e64 v26, v26, 16, s[8:9]
	s_or_b64 exec, exec, s[48:49]
	v_and_b32_e32 v38, 0x20000, v37
	v_cmp_eq_u32_e64 s[8:9], 0, v38
	s_and_saveexec_b64 s[48:49], s[8:9]
	v_cmp_gt_i32_e64 s[8:9], 0, v26
	v_cmp_gt_f32_e64 s[10:11], v17, v36
	s_or_b64 s[8:9], s[8:9], s[10:11]
	v_cndmask_b32_e64 v36, v36, v17, s[8:9]
	v_cndmask_b32_e64 v26, v26, 17, s[8:9]
	s_or_b64 exec, exec, s[48:49]
	v_and_b32_e32 v38, 0x40000, v37
	v_cmp_eq_u32_e64 s[8:9], 0, v38
	s_and_saveexec_b64 s[48:49], s[8:9]
	v_cmp_gt_i32_e64 s[8:9], 0, v26
	v_cmp_gt_f32_e64 s[10:11], v14, v36
	s_or_b64 s[8:9], s[8:9], s[10:11]
	v_cndmask_b32_e64 v36, v36, v14, s[8:9]
	v_cndmask_b32_e64 v26, v26, 18, s[8:9]
	s_or_b64 exec, exec, s[48:49]
	v_and_b32_e32 v38, 0x80000, v37
	v_cmp_eq_u32_e64 s[8:9], 0, v38
	s_and_saveexec_b64 s[48:49], s[8:9]
	v_cmp_gt_i32_e64 s[8:9], 0, v26
	v_cmp_gt_f32_e64 s[10:11], v15, v36
	s_or_b64 s[8:9], s[8:9], s[10:11]
	v_cndmask_b32_e64 v36, v36, v15, s[8:9]
	v_cndmask_b32_e64 v26, v26, 19, s[8:9]
	s_or_b64 exec, exec, s[48:49]
	v_and_b32_e32 v38, 0x100000, v37
	v_cmp_eq_u32_e64 s[8:9], 0, v38
	s_and_saveexec_b64 s[48:49], s[8:9]
	v_cmp_gt_i32_e64 s[8:9], 0, v26
	v_cmp_gt_f32_e64 s[10:11], v12, v36
	s_or_b64 s[8:9], s[8:9], s[10:11]
	v_cndmask_b32_e64 v36, v36, v12, s[8:9]
	v_cndmask_b32_e64 v26, v26, 20, s[8:9]
	s_or_b64 exec, exec, s[48:49]
	v_and_b32_e32 v38, 0x200000, v37
	v_cmp_eq_u32_e64 s[8:9], 0, v38
	s_and_saveexec_b64 s[48:49], s[8:9]
	v_cmp_gt_i32_e64 s[8:9], 0, v26
	v_cmp_gt_f32_e64 s[10:11], v13, v36
	s_or_b64 s[8:9], s[8:9], s[10:11]
	v_cndmask_b32_e64 v36, v36, v13, s[8:9]
	v_cndmask_b32_e64 v26, v26, 21, s[8:9]
	s_or_b64 exec, exec, s[48:49]
	v_and_b32_e32 v38, 0x400000, v37
	v_cmp_eq_u32_e64 s[8:9], 0, v38
	s_and_saveexec_b64 s[48:49], s[8:9]
	v_cmp_gt_i32_e64 s[8:9], 0, v26
	v_cmp_gt_f32_e64 s[10:11], v10, v36
	s_or_b64 s[8:9], s[8:9], s[10:11]
	v_cndmask_b32_e64 v36, v36, v10, s[8:9]
	v_cndmask_b32_e64 v26, v26, 22, s[8:9]
	s_or_b64 exec, exec, s[48:49]
	v_and_b32_e32 v38, 0x800000, v37
	v_cmp_eq_u32_e64 s[8:9], 0, v38
	s_and_saveexec_b64 s[48:49], s[8:9]
	v_cmp_gt_i32_e64 s[8:9], 0, v26
	v_cmp_gt_f32_e64 s[10:11], v11, v36
	s_or_b64 s[8:9], s[8:9], s[10:11]
	v_cndmask_b32_e64 v36, v36, v11, s[8:9]
	v_cndmask_b32_e64 v26, v26, 23, s[8:9]
	s_or_b64 exec, exec, s[48:49]
	v_and_b32_e32 v38, 0x1000000, v37
	v_cmp_eq_u32_e64 s[8:9], 0, v38
	s_and_saveexec_b64 s[48:49], s[8:9]
	v_cmp_gt_i32_e64 s[8:9], 0, v26
	v_cmp_gt_f32_e64 s[10:11], v8, v36
	s_or_b64 s[8:9], s[8:9], s[10:11]
	v_cndmask_b32_e64 v36, v36, v8, s[8:9]
	v_cndmask_b32_e64 v26, v26, 24, s[8:9]
	s_or_b64 exec, exec, s[48:49]
	v_and_b32_e32 v38, 0x2000000, v37
	v_cmp_eq_u32_e64 s[8:9], 0, v38
	s_and_saveexec_b64 s[48:49], s[8:9]
	v_cmp_gt_i32_e64 s[8:9], 0, v26
	v_cmp_gt_f32_e64 s[10:11], v9, v36
	s_or_b64 s[8:9], s[8:9], s[10:11]
	v_cndmask_b32_e64 v36, v36, v9, s[8:9]
	v_cndmask_b32_e64 v26, v26, 25, s[8:9]
	s_or_b64 exec, exec, s[48:49]
	v_and_b32_e32 v38, 0x4000000, v37
	v_cmp_eq_u32_e64 s[8:9], 0, v38
	s_and_saveexec_b64 s[48:49], s[8:9]
	v_cmp_gt_i32_e64 s[8:9], 0, v26
	v_cmp_gt_f32_e64 s[10:11], v6, v36
	s_or_b64 s[8:9], s[8:9], s[10:11]
	v_cndmask_b32_e64 v36, v36, v6, s[8:9]
	v_cndmask_b32_e64 v26, v26, 26, s[8:9]
	s_or_b64 exec, exec, s[48:49]
	v_and_b32_e32 v38, 0x8000000, v37
	v_cmp_eq_u32_e64 s[8:9], 0, v38
	s_and_saveexec_b64 s[48:49], s[8:9]
	v_cmp_gt_i32_e64 s[8:9], 0, v26
	v_cmp_gt_f32_e64 s[10:11], v7, v36
	s_or_b64 s[8:9], s[8:9], s[10:11]
	v_cndmask_b32_e64 v36, v36, v7, s[8:9]
	v_cndmask_b32_e64 v26, v26, 27, s[8:9]
	s_or_b64 exec, exec, s[48:49]
	v_and_b32_e32 v38, 0x10000000, v37
	v_cmp_eq_u32_e64 s[8:9], 0, v38
	s_and_saveexec_b64 s[48:49], s[8:9]
	v_cmp_gt_i32_e64 s[8:9], 0, v26
	v_cmp_gt_f32_e64 s[10:11], v4, v36
	s_or_b64 s[8:9], s[8:9], s[10:11]
	v_cndmask_b32_e64 v36, v36, v4, s[8:9]
	v_cndmask_b32_e64 v26, v26, 28, s[8:9]
	s_or_b64 exec, exec, s[48:49]
	v_and_b32_e32 v38, 0x20000000, v37
	v_cmp_eq_u32_e64 s[8:9], 0, v38
	s_and_saveexec_b64 s[48:49], s[8:9]
	v_cmp_gt_i32_e64 s[8:9], 0, v26
	v_cmp_gt_f32_e64 s[10:11], v5, v36
	s_or_b64 s[8:9], s[8:9], s[10:11]
	v_cndmask_b32_e64 v36, v36, v5, s[8:9]
	v_cndmask_b32_e64 v26, v26, 29, s[8:9]
	s_or_b64 exec, exec, s[48:49]
	v_and_b32_e32 v38, 2.0, v37
	v_cmp_eq_u32_e64 s[8:9], 0, v38
	s_and_saveexec_b64 s[48:49], s[8:9]
	v_cmp_gt_i32_e64 s[8:9], 0, v26
	v_cmp_gt_f32_e64 s[10:11], v2, v36
	s_or_b64 s[8:9], s[8:9], s[10:11]
	v_cndmask_b32_e64 v36, v36, v2, s[8:9]
	v_cndmask_b32_e64 v26, v26, 30, s[8:9]
	s_or_b64 exec, exec, s[48:49]
	v_cmp_lt_i32_e64 s[8:9], -1, v37
	s_and_saveexec_b64 s[48:49], s[8:9]
	v_cmp_gt_i32_e64 s[8:9], 0, v26
	v_cmp_gt_f32_e64 s[10:11], v3, v36
	s_or_b64 s[8:9], s[8:9], s[10:11]
	v_cndmask_b32_e64 v36, v36, v3, s[8:9]
	v_cndmask_b32_e64 v26, v26, 31, s[8:9]
	s_or_b64 exec, exec, s[48:49]
	v_lshlrev_b32_e64 v39, v26, 1
	v_or_b32_e32 v38, v39, v37
	v_and_b32_e32 v40, 1, v38
	v_cmp_eq_u32_e64 s[8:9], 1, v40
	v_bitop3_b32 v42, v39, 2, v37 bitop3:0xc8
	v_bfe_i32 v41, v38, 0, 1
	v_cndmask_b32_e64 v40, v34, 0, s[8:9]
	v_cmp_gt_f32_e64 s[10:11], v35, v40
	s_or_b64 s[8:9], s[8:9], s[10:11]
	v_cndmask_b32_e64 v34, v34, v35, s[8:9]
	v_cndmask_b32_e64 v43, 0, 1, s[8:9]
	v_cmp_eq_u32_e64 s[8:9], 0, v42
	v_bitop3_b32 v37, v39, 4, v37 bitop3:0xc8
	s_nop 0
	v_cndmask_b32_e64 v35, v40, v34, s[8:9]
	v_cndmask_b32_e64 v34, v41, v43, s[8:9]
	v_cmp_eq_u32_e64 s[8:9], 0, v37
	s_and_saveexec_b64 s[48:49], s[8:9]
	v_and_b32_e32 v37, 3, v38
	v_cmp_eq_u32_e64 s[8:9], 3, v37
	v_cmp_gt_f32_e64 s[10:11], v32, v35
	s_or_b64 s[8:9], s[8:9], s[10:11]
	v_cndmask_b32_e64 v35, v35, v32, s[8:9]
	v_cndmask_b32_e64 v34, v34, 2, s[8:9]
	s_or_b64 exec, exec, s[48:49]
	v_and_b32_e32 v32, 8, v38
	v_cmp_eq_u32_e64 s[8:9], 0, v32
	s_and_saveexec_b64 s[48:49], s[8:9]
	v_cmp_gt_i32_e64 s[8:9], 0, v34
	v_cmp_gt_f32_e64 s[10:11], v33, v35
	s_or_b64 s[8:9], s[8:9], s[10:11]
	v_cndmask_b32_e64 v35, v35, v33, s[8:9]
	v_cndmask_b32_e64 v34, v34, 3, s[8:9]
	s_or_b64 exec, exec, s[48:49]
	v_and_b32_e32 v32, 16, v38
	v_cmp_eq_u32_e64 s[8:9], 0, v32
	s_and_saveexec_b64 s[48:49], s[8:9]
	v_cmp_gt_i32_e64 s[8:9], 0, v34
	v_cmp_gt_f32_e64 s[10:11], v30, v35
	s_or_b64 s[8:9], s[8:9], s[10:11]
	v_cndmask_b32_e64 v35, v35, v30, s[8:9]
	v_cndmask_b32_e64 v34, v34, 4, s[8:9]
	s_or_b64 exec, exec, s[48:49]
	v_and_b32_e32 v30, 32, v38
	v_cmp_eq_u32_e64 s[8:9], 0, v30
	s_and_saveexec_b64 s[48:49], s[8:9]
	v_cmp_gt_i32_e64 s[8:9], 0, v34
	v_cmp_gt_f32_e64 s[10:11], v31, v35
	s_or_b64 s[8:9], s[8:9], s[10:11]
	v_cndmask_b32_e64 v35, v35, v31, s[8:9]
	v_cndmask_b32_e64 v34, v34, 5, s[8:9]
	s_or_b64 exec, exec, s[48:49]
	v_and_b32_e32 v30, 64, v38
	v_cmp_eq_u32_e64 s[8:9], 0, v30
	s_and_saveexec_b64 s[48:49], s[8:9]
	v_cmp_gt_i32_e64 s[8:9], 0, v34
	v_cmp_gt_f32_e64 s[10:11], v28, v35
	s_or_b64 s[8:9], s[8:9], s[10:11]
	v_cndmask_b32_e64 v35, v35, v28, s[8:9]
	v_cndmask_b32_e64 v34, v34, 6, s[8:9]
	s_or_b64 exec, exec, s[48:49]
	v_and_b32_e32 v28, 0x80, v38
	v_cmp_eq_u32_e64 s[8:9], 0, v28
	s_and_saveexec_b64 s[48:49], s[8:9]
	v_cmp_gt_i32_e64 s[8:9], 0, v34
	v_cmp_gt_f32_e64 s[10:11], v29, v35
	s_or_b64 s[8:9], s[8:9], s[10:11]
	v_cndmask_b32_e64 v35, v35, v29, s[8:9]
	v_cndmask_b32_e64 v34, v34, 7, s[8:9]
	s_or_b64 exec, exec, s[48:49]
	v_and_b32_e32 v28, 0x100, v38
	v_cmp_eq_u32_e64 s[8:9], 0, v28
	s_and_saveexec_b64 s[48:49], s[8:9]
	v_cmp_gt_i32_e64 s[8:9], 0, v34
	v_cmp_gt_f32_e64 s[10:11], v24, v35
	s_or_b64 s[8:9], s[8:9], s[10:11]
	v_cndmask_b32_e64 v35, v35, v24, s[8:9]
	v_cndmask_b32_e64 v34, v34, 8, s[8:9]
	s_or_b64 exec, exec, s[48:49]
	v_and_b32_e32 v24, 0x200, v38
	v_cmp_eq_u32_e64 s[8:9], 0, v24
	s_and_saveexec_b64 s[48:49], s[8:9]
	v_cmp_gt_i32_e64 s[8:9], 0, v34
	v_cmp_gt_f32_e64 s[10:11], v25, v35
	s_or_b64 s[8:9], s[8:9], s[10:11]
	v_cndmask_b32_e64 v35, v35, v25, s[8:9]
	v_cndmask_b32_e64 v34, v34, 9, s[8:9]
	s_or_b64 exec, exec, s[48:49]
	v_and_b32_e32 v24, 0x400, v38
	v_cmp_eq_u32_e64 s[8:9], 0, v24
	s_and_saveexec_b64 s[48:49], s[8:9]
	v_cmp_gt_i32_e64 s[8:9], 0, v34
	v_cmp_gt_f32_e64 s[10:11], v22, v35
	s_or_b64 s[8:9], s[8:9], s[10:11]
	v_cndmask_b32_e64 v35, v35, v22, s[8:9]
	v_cndmask_b32_e64 v34, v34, 10, s[8:9]
	s_or_b64 exec, exec, s[48:49]
	v_and_b32_e32 v22, 0x800, v38
	v_cmp_eq_u32_e64 s[8:9], 0, v22
	s_and_saveexec_b64 s[48:49], s[8:9]
	v_cmp_gt_i32_e64 s[8:9], 0, v34
	v_cmp_gt_f32_e64 s[10:11], v23, v35
	s_or_b64 s[8:9], s[8:9], s[10:11]
	v_cndmask_b32_e64 v35, v35, v23, s[8:9]
	v_cndmask_b32_e64 v34, v34, 11, s[8:9]
	s_or_b64 exec, exec, s[48:49]
	v_and_b32_e32 v22, 0x1000, v38
	v_cmp_eq_u32_e64 s[8:9], 0, v22
	s_and_saveexec_b64 s[48:49], s[8:9]
	v_cmp_gt_i32_e64 s[8:9], 0, v34
	v_cmp_gt_f32_e64 s[10:11], v20, v35
	s_or_b64 s[8:9], s[8:9], s[10:11]
	v_cndmask_b32_e64 v35, v35, v20, s[8:9]
	v_cndmask_b32_e64 v34, v34, 12, s[8:9]
	s_or_b64 exec, exec, s[48:49]
	v_and_b32_e32 v20, 0x2000, v38
	v_cmp_eq_u32_e64 s[8:9], 0, v20
	s_and_saveexec_b64 s[48:49], s[8:9]
	v_cmp_gt_i32_e64 s[8:9], 0, v34
	v_cmp_gt_f32_e64 s[10:11], v21, v35
	s_or_b64 s[8:9], s[8:9], s[10:11]
	v_cndmask_b32_e64 v35, v35, v21, s[8:9]
	v_cndmask_b32_e64 v34, v34, 13, s[8:9]
	s_or_b64 exec, exec, s[48:49]
	v_and_b32_e32 v20, 0x4000, v38
	v_cmp_eq_u32_e64 s[8:9], 0, v20
	s_and_saveexec_b64 s[48:49], s[8:9]
	v_cmp_gt_i32_e64 s[8:9], 0, v34
	v_cmp_gt_f32_e64 s[10:11], v18, v35
	s_or_b64 s[8:9], s[8:9], s[10:11]
	v_cndmask_b32_e64 v35, v35, v18, s[8:9]
	v_cndmask_b32_e64 v34, v34, 14, s[8:9]
	s_or_b64 exec, exec, s[48:49]
	v_and_b32_e32 v18, 0x8000, v38
	v_cmp_eq_u32_e64 s[8:9], 0, v18
	s_and_saveexec_b64 s[48:49], s[8:9]
	v_cmp_gt_i32_e64 s[8:9], 0, v34
	v_cmp_gt_f32_e64 s[10:11], v19, v35
	s_or_b64 s[8:9], s[8:9], s[10:11]
	v_cndmask_b32_e64 v35, v35, v19, s[8:9]
	v_cndmask_b32_e64 v34, v34, 15, s[8:9]
	s_or_b64 exec, exec, s[48:49]
	v_and_b32_e32 v18, 0x10000, v38
	v_cmp_eq_u32_e64 s[8:9], 0, v18
	s_and_saveexec_b64 s[48:49], s[8:9]
	v_cmp_gt_i32_e64 s[8:9], 0, v34
	v_cmp_gt_f32_e64 s[10:11], v16, v35
	s_or_b64 s[8:9], s[8:9], s[10:11]
	v_cndmask_b32_e64 v35, v35, v16, s[8:9]
	v_cndmask_b32_e64 v34, v34, 16, s[8:9]
	s_or_b64 exec, exec, s[48:49]
	v_and_b32_e32 v16, 0x20000, v38
	v_cmp_eq_u32_e64 s[8:9], 0, v16
	s_and_saveexec_b64 s[48:49], s[8:9]
	v_cmp_gt_i32_e64 s[8:9], 0, v34
	v_cmp_gt_f32_e64 s[10:11], v17, v35
	s_or_b64 s[8:9], s[8:9], s[10:11]
	v_cndmask_b32_e64 v35, v35, v17, s[8:9]
	v_cndmask_b32_e64 v34, v34, 17, s[8:9]
	s_or_b64 exec, exec, s[48:49]
	v_and_b32_e32 v16, 0x40000, v38
	v_cmp_eq_u32_e64 s[8:9], 0, v16
	s_and_saveexec_b64 s[48:49], s[8:9]
	v_cmp_gt_i32_e64 s[8:9], 0, v34
	v_cmp_gt_f32_e64 s[10:11], v14, v35
	s_or_b64 s[8:9], s[8:9], s[10:11]
	v_cndmask_b32_e64 v35, v35, v14, s[8:9]
	v_cndmask_b32_e64 v34, v34, 18, s[8:9]
	s_or_b64 exec, exec, s[48:49]
	v_and_b32_e32 v14, 0x80000, v38
	v_cmp_eq_u32_e64 s[8:9], 0, v14
	s_and_saveexec_b64 s[48:49], s[8:9]
	v_cmp_gt_i32_e64 s[8:9], 0, v34
	v_cmp_gt_f32_e64 s[10:11], v15, v35
	s_or_b64 s[8:9], s[8:9], s[10:11]
	v_cndmask_b32_e64 v35, v35, v15, s[8:9]
	v_cndmask_b32_e64 v34, v34, 19, s[8:9]
	s_or_b64 exec, exec, s[48:49]
	v_and_b32_e32 v14, 0x100000, v38
	v_cmp_eq_u32_e64 s[8:9], 0, v14
	s_and_saveexec_b64 s[48:49], s[8:9]
	v_cmp_gt_i32_e64 s[8:9], 0, v34
	v_cmp_gt_f32_e64 s[10:11], v12, v35
	s_or_b64 s[8:9], s[8:9], s[10:11]
	v_cndmask_b32_e64 v35, v35, v12, s[8:9]
	v_cndmask_b32_e64 v34, v34, 20, s[8:9]
	s_or_b64 exec, exec, s[48:49]
	v_and_b32_e32 v12, 0x200000, v38
	v_cmp_eq_u32_e64 s[8:9], 0, v12
	s_and_saveexec_b64 s[48:49], s[8:9]
	v_cmp_gt_i32_e64 s[8:9], 0, v34
	v_cmp_gt_f32_e64 s[10:11], v13, v35
	s_or_b64 s[8:9], s[8:9], s[10:11]
	v_cndmask_b32_e64 v35, v35, v13, s[8:9]
	v_cndmask_b32_e64 v34, v34, 21, s[8:9]
	s_or_b64 exec, exec, s[48:49]
	v_and_b32_e32 v12, 0x400000, v38
	v_cmp_eq_u32_e64 s[8:9], 0, v12
	s_and_saveexec_b64 s[48:49], s[8:9]
	v_cmp_gt_i32_e64 s[8:9], 0, v34
	v_cmp_gt_f32_e64 s[10:11], v10, v35
	s_or_b64 s[8:9], s[8:9], s[10:11]
	v_cndmask_b32_e64 v35, v35, v10, s[8:9]
	v_cndmask_b32_e64 v34, v34, 22, s[8:9]
	s_or_b64 exec, exec, s[48:49]
	v_and_b32_e32 v10, 0x800000, v38
	v_cmp_eq_u32_e64 s[8:9], 0, v10
	s_and_saveexec_b64 s[48:49], s[8:9]
	v_cmp_gt_i32_e64 s[8:9], 0, v34
	v_cmp_gt_f32_e64 s[10:11], v11, v35
	s_or_b64 s[8:9], s[8:9], s[10:11]
	v_cndmask_b32_e64 v35, v35, v11, s[8:9]
	v_cndmask_b32_e64 v34, v34, 23, s[8:9]
	s_or_b64 exec, exec, s[48:49]
	v_and_b32_e32 v10, 0x1000000, v38
	v_cmp_eq_u32_e64 s[8:9], 0, v10
	s_and_saveexec_b64 s[48:49], s[8:9]
	v_cmp_gt_i32_e64 s[8:9], 0, v34
	v_cmp_gt_f32_e64 s[10:11], v8, v35
	s_or_b64 s[8:9], s[8:9], s[10:11]
	v_cndmask_b32_e64 v35, v35, v8, s[8:9]
	v_cndmask_b32_e64 v34, v34, 24, s[8:9]
	s_or_b64 exec, exec, s[48:49]
	v_and_b32_e32 v8, 0x2000000, v38
	v_cmp_eq_u32_e64 s[8:9], 0, v8
	s_and_saveexec_b64 s[48:49], s[8:9]
	v_cmp_gt_i32_e64 s[8:9], 0, v34
	v_cmp_gt_f32_e64 s[10:11], v9, v35
	s_or_b64 s[8:9], s[8:9], s[10:11]
	v_cndmask_b32_e64 v35, v35, v9, s[8:9]
	v_cndmask_b32_e64 v34, v34, 25, s[8:9]
	s_or_b64 exec, exec, s[48:49]
	v_and_b32_e32 v8, 0x4000000, v38
	v_cmp_eq_u32_e64 s[8:9], 0, v8
	s_and_saveexec_b64 s[48:49], s[8:9]
	v_cmp_gt_i32_e64 s[8:9], 0, v34
	v_cmp_gt_f32_e64 s[10:11], v6, v35
	s_or_b64 s[8:9], s[8:9], s[10:11]
	v_cndmask_b32_e64 v35, v35, v6, s[8:9]
	v_cndmask_b32_e64 v34, v34, 26, s[8:9]
	s_or_b64 exec, exec, s[48:49]
	v_and_b32_e32 v6, 0x8000000, v38
	v_cmp_eq_u32_e64 s[8:9], 0, v6
	s_and_saveexec_b64 s[48:49], s[8:9]
	v_cmp_gt_i32_e64 s[8:9], 0, v34
	v_cmp_gt_f32_e64 s[10:11], v7, v35
	s_or_b64 s[8:9], s[8:9], s[10:11]
	v_cndmask_b32_e64 v35, v35, v7, s[8:9]
	v_cndmask_b32_e64 v34, v34, 27, s[8:9]
	s_or_b64 exec, exec, s[48:49]
	v_and_b32_e32 v6, 0x10000000, v38
	v_cmp_eq_u32_e64 s[8:9], 0, v6
	s_and_saveexec_b64 s[48:49], s[8:9]
	v_cmp_gt_i32_e64 s[8:9], 0, v34
	v_cmp_gt_f32_e64 s[10:11], v4, v35
	s_or_b64 s[8:9], s[8:9], s[10:11]
	v_cndmask_b32_e64 v35, v35, v4, s[8:9]
	v_cndmask_b32_e64 v34, v34, 28, s[8:9]
	s_or_b64 exec, exec, s[48:49]
	v_and_b32_e32 v4, 0x20000000, v38
	v_cmp_eq_u32_e64 s[8:9], 0, v4
	s_and_saveexec_b64 s[48:49], s[8:9]
	v_cmp_gt_i32_e64 s[8:9], 0, v34
	v_cmp_gt_f32_e64 s[10:11], v5, v35
	s_or_b64 s[8:9], s[8:9], s[10:11]
	v_cndmask_b32_e64 v35, v35, v5, s[8:9]
	v_cndmask_b32_e64 v34, v34, 29, s[8:9]
	s_or_b64 exec, exec, s[48:49]
	v_and_b32_e32 v4, 2.0, v38
	v_cmp_eq_u32_e64 s[8:9], 0, v4
	s_and_saveexec_b64 s[48:49], s[8:9]
	v_cmp_gt_i32_e64 s[8:9], 0, v34
	v_cmp_gt_f32_e64 s[10:11], v2, v35
	s_or_b64 s[8:9], s[8:9], s[10:11]
	v_cndmask_b32_e64 v35, v35, v2, s[8:9]
	v_cndmask_b32_e64 v34, v34, 30, s[8:9]
	s_or_b64 exec, exec, s[48:49]
	v_cmp_lt_i32_e64 s[8:9], -1, v38
	s_and_saveexec_b64 s[48:49], s[8:9]
	v_cmp_gt_i32_e64 s[8:9], 0, v34
	v_cmp_gt_f32_e64 s[10:11], v3, v35
	s_or_b64 s[8:9], s[8:9], s[10:11]
	v_cndmask_b32_e64 v35, v35, v3, s[8:9]
	v_cndmask_b32_e64 v34, v34, 31, s[8:9]
	s_or_b64 exec, exec, s[48:49]
	v_cndmask_b32_e32 v1, v1, v3, vcc
	v_sub_f32_e32 v2, v1, v1
	v_mul_f32_e32 v2, 0x3fb8aa3b, v2
	v_sub_f32_e32 v3, v27, v1
	v_exp_f32_e32 v2, v2
	v_mul_f32_e32 v3, 0x3fb8aa3b, v3
	v_sub_f32_e32 v4, v36, v1
	v_exp_f32_e32 v3, v3
	v_mul_f32_e32 v4, 0x3fb8aa3b, v4
	v_sub_f32_e32 v1, v35, v1
	v_exp_f32_e32 v8, v4
	v_mul_f32_e32 v1, 0x3fb8aa3b, v1
	v_exp_f32_e32 v9, v1
	v_add_f32_e32 v1, 0, v2
	v_add_f32_e32 v1, v1, v3
	v_add_f32_e32 v1, v1, v8
	v_add_f32_e32 v7, v1, v9
	v_div_scale_f32 v1, s[0:1], v7, v7, 1.0
	v_rcp_f32_e32 v10, v1
	s_nop 0
	v_fma_f32 v4, -v1, v10, 1.0
	v_fmac_f32_e32 v10, v4, v10
	v_div_scale_f32 v4, vcc, 1.0, v7, 1.0
	v_mul_f32_e32 v11, v4, v10
	v_fma_f32 v5, -v1, v11, v4
	v_fmac_f32_e32 v11, v5, v10
	v_fma_f32 v12, -v1, v11, v4
	v_lshl_add_u32 v1, v200, 2, 0
	ds_add_rtn_u32 v1, v1, v225 offset:20480
	v_lshl_add_u32 v4, v0, 2, 0
	ds_add_rtn_u32 v6, v4, v225 offset:20480
	v_lshl_add_u32 v4, v26, 2, 0
	ds_add_rtn_u32 v5, v4, v225 offset:20480
	v_lshl_add_u32 v4, v34, 2, 0
	ds_add_rtn_u32 v4, v4, v225 offset:20480
	v_div_fmas_f32 v10, v12, v10, v11
	v_div_fixup_f32 v10, v10, v7, 1.0
	v_pk_mul_f32 v[2:3], v[10:11], v[2:3] op_sel_hi:[0,1]
	v_pk_mul_f32 v[196:197], v[10:11], v[8:9] op_sel_hi:[0,1]
